# speedup vs baseline: 1.0403x; 1.0194x over previous
.LBB3_35:
	s_andn2_b64 vcc, exec, s[2:3]
	s_cbranch_vccnz .LBB3_39
	s_waitcnt vmcnt(4)
	v_ashrrev_i32_e32 v81, 31, v80
	v_lshl_add_u64 v[2:3], v[80:81], 3, s[20:21]
	v_add_co_u32_e32 v2, vcc, 0x48000, v2
	s_movk_i32 s8, 0x620
	s_nop 0
	v_addc_co_u32_e32 v3, vcc, 0, v3, vcc
	global_load_dwordx2 v[82:83], v[2:3], off
	v_and_b32_e32 v2, 0x70, v7
	v_bitop3_b32 v2, v0, v2, 48 bitop3:0x6c
	s_waitcnt vmcnt(4)
	v_mad_u64_u32 v[64:65], s[6:7], v9, s8, v[2:3]
	v_lshrrev_b32_e32 v3, 4, v92
	v_bitop3_b32 v3, v3, v0, 4 bitop3:0x36
	v_lshlrev_b32_e32 v3, 4, v3
	v_and_b32_e32 v4, 0x70, v3
	s_waitcnt vmcnt(3)
	v_mad_u64_u32 v[66:67], s[6:7], v8, s8, v[4:5]
	s_waitcnt vmcnt(2)
	v_mad_u64_u32 v[68:69], s[6:7], v6, s8, v[2:3]
	s_waitcnt vmcnt(1)
	v_mad_u64_u32 v[70:71], s[6:7], v1, s8, v[4:5]
	v_lshrrev_b32_e32 v85, 5, v92
	v_bfe_u32 v2, v0, 1, 3
	s_mov_b64 s[6:7], 0x1800
	s_add_u32 s4, s20, 0x4000000
	v_bitop3_b32 v32, v85, v2, 2 bitop3:0x36
	v_bitop3_b32 v33, v85, v2, 4 bitop3:0x36
	v_bitop3_b32 v34, v85, v2, 6 bitop3:0x36
	v_lshl_add_u64 v[2:3], v[86:87], 0, s[6:7]
	s_addc_u32 s5, s21, 0
	s_lshl_b32 s2, s27, 12
	s_addk_i32 s2, 0x6000
	v_lshrrev_b32_e32 v1, 1, v0
	v_or_b32_e32 v81, s2, v84
	v_lshlrev_b32_e32 v0, 7, v0
	v_and_b32_e32 v8, 0xf80, v0
	v_lshlrev_b32_e32 v9, 4, v32
	v_bitop3_b32 v1, v85, v1, 7 bitop3:0x78
	v_or3_b32 v96, s2, v9, v8
	v_lshlrev_b32_e32 v9, 4, v33
	v_lshlrev_b32_e32 v1, 4, v1
	v_or3_b32 v97, s2, v9, v8
	v_lshlrev_b32_e32 v9, 4, v34
	v_or3_b32 v95, s2, v1, v8
	v_or3_b32 v94, s2, v9, v8
	v_add_u32_e32 v98, 0x103c0, v84
	global_load_dwordx4 v[116:119], v64, s[4:5] offset:0
	global_load_dwordx4 v[120:123], v66, s[4:5] offset:0
	global_load_dwordx4 v[124:127], v68, s[4:5] offset:0
	global_load_dwordx4 v[128:131], v70, s[4:5] offset:0
	global_load_dwordx4 v[132:135], v64, s[4:5] offset:128
	global_load_dwordx4 v[136:139], v66, s[4:5] offset:128
	global_load_dwordx4 v[140:143], v68, s[4:5] offset:128
	global_load_dwordx4 v[144:147], v70, s[4:5] offset:128
	global_load_dwordx4 v[148:151], v64, s[4:5] offset:256
	global_load_dwordx4 v[152:155], v66, s[4:5] offset:256
	global_load_dwordx4 v[156:159], v68, s[4:5] offset:256
	global_load_dwordx4 v[72:75], v70, s[4:5] offset:256
	s_add_u32 m0, s46, 0x0
	s_nop 0
	global_load_lds_dwordx4 v76, s[40:41]
	s_add_u32 m0, s47, 0x0
	s_nop 0
	global_load_lds_dwordx4 v77, s[42:43]
	s_add_u32 m0, s48, 0x0
	s_nop 0
	global_load_lds_dwordx4 v78, s[44:45]
	s_add_u32 m0, s46, 0x3000
	s_add_u32 s40, s40, 0x1800
	s_addc_u32 s41, s41, 0
	global_load_lds_dwordx4 v76, s[40:41]
	s_add_u32 m0, s47, 0x3000
	s_add_u32 s42, s42, 0x1800
	s_addc_u32 s43, s43, 0
	global_load_lds_dwordx4 v77, s[42:43]
	s_add_u32 m0, s48, 0x3000
	s_add_u32 s44, s44, 0x1800
	s_addc_u32 s45, s45, 0
	global_load_lds_dwordx4 v78, s[44:45]
	s_add_u32 m0, s46, 0xd3c0
	s_add_u32 s40, s40, 0x1800
	s_addc_u32 s41, s41, 0
	global_load_lds_dwordx4 v76, s[40:41]
	s_add_u32 m0, s47, 0xd3c0
	s_add_u32 s42, s42, 0x1800
	s_addc_u32 s43, s43, 0
	global_load_lds_dwordx4 v77, s[42:43]
	s_add_u32 m0, s48, 0xd3c0
	s_add_u32 s44, s44, 0x1800
	s_addc_u32 s45, s45, 0
	global_load_lds_dwordx4 v78, s[44:45]
	s_add_u32 m0, s46, 0x103c0
	s_add_u32 s40, s40, 0x1800
	s_addc_u32 s41, s41, 0
	global_load_lds_dwordx4 v76, s[40:41]
	s_add_u32 m0, s47, 0x103c0
	s_add_u32 s42, s42, 0x1800
	s_addc_u32 s43, s43, 0
	global_load_lds_dwordx4 v77, s[42:43]
	s_add_u32 m0, s48, 0x103c0
	s_add_u32 s44, s44, 0x1800
	s_addc_u32 s45, s45, 0
	global_load_lds_dwordx4 v78, s[44:45]
	s_waitcnt vmcnt(20)
	ds_write_b128 v81, v[116:119]
	ds_write_b128 v81, v[120:123] offset:1024
	ds_write_b128 v81, v[124:127] offset:2048
	ds_write_b128 v81, v[128:131] offset:3072
	ds_read_b128 v[52:55], v95
	ds_read_b128 v[56:59], v96
	ds_read_b128 v[60:63], v97
	ds_read_b128 v[0:3], v94
	global_load_dwordx4 v[116:119], v64, s[4:5] offset:384
	global_load_dwordx4 v[120:123], v66, s[4:5] offset:384
	global_load_dwordx4 v[124:127], v68, s[4:5] offset:384
	global_load_dwordx4 v[128:131], v70, s[4:5] offset:384
	s_waitcnt vmcnt(13)
	s_waitcnt lgkmcnt(0)
	s_barrier
	ds_read_b128 v[4:7], v84 offset:0
	ds_read_b128 v[8:11], v84 offset:1024
	ds_read_b128 v[12:15], v84 offset:2048
	ds_read_b128 v[16:19], v84 offset:3072
	ds_read_b128 v[20:23], v84 offset:4096
	ds_read_b128 v[24:27], v84 offset:5120
	ds_read_b128 v[28:31], v84 offset:6144
	ds_read_b128 v[32:35], v84 offset:7168
	ds_read_b128 v[36:39], v84 offset:8192
	ds_read_b128 v[40:43], v84 offset:9216
	ds_read_b128 v[44:47], v84 offset:10240
	ds_read_b128 v[48:51], v84 offset:11264
	s_waitcnt lgkmcnt(6)
	v_mfma_f32_32x32x16_f16 a[80:95], v[4:7], v[52:55], 0
	v_mfma_f32_32x32x16_f16 a[64:79], v[8:11], v[52:55], 0
	v_mfma_f32_32x32x16_f16 a[48:63], v[12:15], v[52:55], 0
	s_waitcnt vmcnt(10)
	s_waitcnt lgkmcnt(0)
	s_barrier
	ds_read_b128 v[4:7], v84 offset:12288
	ds_read_b128 v[8:11], v84 offset:13312
	ds_read_b128 v[12:15], v84 offset:14336
	s_nop 0
	v_mfma_f32_32x32x16_f16 a[32:47], v[16:19], v[52:55], 0
	ds_read_b128 v[16:19], v84 offset:15360
	v_mfma_f32_32x32x16_f16 a[16:31], v[20:23], v[52:55], 0
	ds_read_b128 v[20:23], v84 offset:16384
	v_mfma_f32_32x32x16_f16 a[0:15], v[24:27], v[52:55], 0
	ds_read_b128 v[24:27], v84 offset:17408
	v_mfma_f32_32x32x16_f16 a[80:95], v[28:31], v[56:59], a[80:95]
	s_add_u32 m0, s46, 0x0
	s_add_u32 s40, s40, 0x1800
	s_addc_u32 s41, s41, 0
	global_load_lds_dwordx4 v76, s[40:41]
	ds_read_b128 v[28:31], v84 offset:18432
	v_mfma_f32_32x32x16_f16 a[64:79], v[32:35], v[56:59], a[64:79]
	ds_read_b128 v[32:35], v84 offset:19456
	v_mfma_f32_32x32x16_f16 a[48:63], v[36:39], v[56:59], a[48:63]
	s_add_u32 m0, s47, 0x0
	s_add_u32 s42, s42, 0x1800
	s_addc_u32 s43, s43, 0
	global_load_lds_dwordx4 v77, s[42:43]
	ds_read_b128 v[36:39], v84 offset:20480
	v_mfma_f32_32x32x16_f16 a[32:47], v[40:43], v[56:59], a[32:47]
	ds_read_b128 v[40:43], v84 offset:21504
	v_mfma_f32_32x32x16_f16 a[16:31], v[44:47], v[56:59], a[16:31]
	s_add_u32 m0, s48, 0x0
	s_add_u32 s44, s44, 0x1800
	s_addc_u32 s45, s45, 0
	global_load_lds_dwordx4 v78, s[44:45]
	ds_read_b128 v[44:47], v84 offset:22528
	v_mfma_f32_32x32x16_f16 a[0:15], v[48:51], v[56:59], a[0:15]
	ds_read_b128 v[48:51], v84 offset:23552
	s_waitcnt lgkmcnt(6)
	s_nop 0
	v_mfma_f32_32x32x16_f16 a[80:95], v[4:7], v[60:63], a[80:95]
	s_waitcnt vmcnt(23)
	ds_write_b128 v81, v[132:135]
	ds_write_b128 v81, v[136:139] offset:1024
	ds_write_b128 v81, v[140:143] offset:2048
	ds_write_b128 v81, v[144:147] offset:3072
	s_nop 0
	v_mfma_f32_32x32x16_f16 a[64:79], v[8:11], v[60:63], a[64:79]
	ds_read_b128 v[100:103], v95
	ds_read_b128 v[104:107], v96
	ds_read_b128 v[108:111], v97
	ds_read_b128 v[112:115], v94
	v_mfma_f32_32x32x16_f16 a[48:63], v[12:15], v[60:63], a[48:63]
	global_load_dwordx4 v[132:135], v64, s[4:5] offset:512
	global_load_dwordx4 v[136:139], v66, s[4:5] offset:512
	global_load_dwordx4 v[140:143], v68, s[4:5] offset:512
	global_load_dwordx4 v[144:147], v70, s[4:5] offset:512
	s_waitcnt vmcnt(14)
	s_waitcnt lgkmcnt(8)
	s_barrier
	ds_read_b128 v[4:7], v84 offset:54208
	ds_read_b128 v[8:11], v84 offset:55232
	ds_read_b128 v[12:15], v84 offset:56256
	s_nop 0
	v_mfma_f32_32x32x16_f16 a[32:47], v[16:19], v[60:63], a[32:47]
	ds_read_b128 v[16:19], v84 offset:57280
	v_mfma_f32_32x32x16_f16 a[16:31], v[20:23], v[60:63], a[16:31]
	ds_read_b128 v[20:23], v84 offset:58304
	v_mfma_f32_32x32x16_f16 a[0:15], v[24:27], v[60:63], a[0:15]
	ds_read_b128 v[24:27], v84 offset:59328
	s_waitcnt lgkmcnt(6)
	s_nop 0
	v_mfma_f32_32x32x16_f16 a[80:95], v[28:31], v[0:3], a[80:95]
	s_add_u32 m0, s46, 0x3000
	s_add_u32 s40, s40, 0x1800
	s_addc_u32 s41, s41, 0
	global_load_lds_dwordx4 v76, s[40:41]
	ds_read_b128 v[28:31], v84 offset:60352
	s_nop 0
	v_mfma_f32_32x32x16_f16 a[64:79], v[32:35], v[0:3], a[64:79]
	ds_read_b128 v[32:35], v84 offset:61376
	v_mfma_f32_32x32x16_f16 a[48:63], v[36:39], v[0:3], a[48:63]
	s_add_u32 m0, s47, 0x3000
	s_add_u32 s42, s42, 0x1800
	s_addc_u32 s43, s43, 0
	global_load_lds_dwordx4 v77, s[42:43]
	ds_read_b128 v[36:39], v84 offset:62400
	s_nop 0
	v_mfma_f32_32x32x16_f16 a[32:47], v[40:43], v[0:3], a[32:47]
	ds_read_b128 v[40:43], v84 offset:63424
	v_mfma_f32_32x32x16_f16 a[16:31], v[44:47], v[0:3], a[16:31]
	s_add_u32 m0, s48, 0x3000
	s_add_u32 s44, s44, 0x1800
	s_addc_u32 s45, s45, 0
	global_load_lds_dwordx4 v78, s[44:45]
	ds_read_b128 v[44:47], v84 offset:64448
	s_nop 0
	v_mfma_f32_32x32x16_f16 a[0:15], v[48:51], v[0:3], a[0:15]
	ds_read_b128 v[48:51], v84 offset:65472
	s_waitcnt lgkmcnt(6)
	s_nop 0
	v_mfma_f32_32x32x16_f16 a[80:95], v[4:7], v[100:103], a[80:95]
	v_mfma_f32_32x32x16_f16 a[64:79], v[8:11], v[100:103], a[64:79]
	v_mfma_f32_32x32x16_f16 a[48:63], v[12:15], v[100:103], a[48:63]
	s_waitcnt vmcnt(14)
	s_waitcnt lgkmcnt(0)
	s_barrier
	ds_read_b128 v[4:7], v98
	ds_read_b128 v[8:11], v98 offset:1024
	ds_read_b128 v[12:15], v98 offset:2048
	s_nop 0
	v_mfma_f32_32x32x16_f16 a[32:47], v[16:19], v[100:103], a[32:47]
	ds_read_b128 v[16:19], v98 offset:3072
	v_mfma_f32_32x32x16_f16 a[16:31], v[20:23], v[100:103], a[16:31]
	ds_read_b128 v[20:23], v98 offset:4096
	v_mfma_f32_32x32x16_f16 a[0:15], v[24:27], v[100:103], a[0:15]
	ds_read_b128 v[24:27], v98 offset:5120
	v_mfma_f32_32x32x16_f16 a[80:95], v[28:31], v[104:107], a[80:95]
	s_add_u32 m0, s46, 0xd3c0
	s_add_u32 s40, s40, 0x1800
	s_addc_u32 s41, s41, 0
	global_load_lds_dwordx4 v76, s[40:41]
	ds_read_b128 v[28:31], v98 offset:6144
	s_nop 0
	v_mfma_f32_32x32x16_f16 a[64:79], v[32:35], v[104:107], a[64:79]
	ds_read_b128 v[32:35], v98 offset:7168
	v_mfma_f32_32x32x16_f16 a[48:63], v[36:39], v[104:107], a[48:63]
	s_add_u32 m0, s47, 0xd3c0
	s_add_u32 s42, s42, 0x1800
	s_addc_u32 s43, s43, 0
	global_load_lds_dwordx4 v77, s[42:43]
	ds_read_b128 v[36:39], v98 offset:8192
	s_nop 0
	v_mfma_f32_32x32x16_f16 a[32:47], v[40:43], v[104:107], a[32:47]
	ds_read_b128 v[40:43], v98 offset:9216
	v_mfma_f32_32x32x16_f16 a[16:31], v[44:47], v[104:107], a[16:31]
	s_add_u32 m0, s48, 0xd3c0
	s_add_u32 s44, s44, 0x1800
	s_addc_u32 s45, s45, 0
	global_load_lds_dwordx4 v78, s[44:45]
	ds_read_b128 v[44:47], v98 offset:10240
	s_nop 0
	v_mfma_f32_32x32x16_f16 a[0:15], v[48:51], v[104:107], a[0:15]
	ds_read_b128 v[48:51], v98 offset:11264
	s_waitcnt lgkmcnt(6)
	s_nop 0
	v_mfma_f32_32x32x16_f16 a[80:95], v[4:7], v[108:111], a[80:95]
	s_waitcnt vmcnt(29)
	ds_write_b128 v81, v[148:151]
	ds_write_b128 v81, v[152:155] offset:1024
	ds_write_b128 v81, v[156:159] offset:2048
	ds_write_b128 v81, v[72:75] offset:3072
	s_nop 0
	v_mfma_f32_32x32x16_f16 a[64:79], v[8:11], v[108:111], a[64:79]
	ds_read_b128 v[52:55], v95
	ds_read_b128 v[56:59], v96
	ds_read_b128 v[60:63], v97
	ds_read_b128 v[0:3], v94
	v_mfma_f32_32x32x16_f16 a[48:63], v[12:15], v[108:111], a[48:63]
	global_load_dwordx4 v[148:151], v64, s[4:5] offset:640
	global_load_dwordx4 v[152:155], v66, s[4:5] offset:640
	global_load_dwordx4 v[156:159], v68, s[4:5] offset:640
	global_load_dwordx4 v[72:75], v70, s[4:5] offset:640
	s_waitcnt vmcnt(14)
	s_waitcnt lgkmcnt(8)
	s_barrier
	ds_read_b128 v[4:7], v84 offset:0
	ds_read_b128 v[8:11], v84 offset:1024
	ds_read_b128 v[12:15], v84 offset:2048
	s_nop 0
	v_mfma_f32_32x32x16_f16 a[32:47], v[16:19], v[108:111], a[32:47]
	ds_read_b128 v[16:19], v84 offset:3072
	v_mfma_f32_32x32x16_f16 a[16:31], v[20:23], v[108:111], a[16:31]
	ds_read_b128 v[20:23], v84 offset:4096
	v_mfma_f32_32x32x16_f16 a[0:15], v[24:27], v[108:111], a[0:15]
	ds_read_b128 v[24:27], v84 offset:5120
	s_waitcnt lgkmcnt(6)
	s_nop 0
	v_mfma_f32_32x32x16_f16 a[80:95], v[28:31], v[112:115], a[80:95]
	s_add_u32 m0, s46, 0x103c0
	s_add_u32 s40, s40, 0x1800
	s_addc_u32 s41, s41, 0
	global_load_lds_dwordx4 v76, s[40:41]
	ds_read_b128 v[28:31], v84 offset:6144
	s_nop 0
	v_mfma_f32_32x32x16_f16 a[64:79], v[32:35], v[112:115], a[64:79]
	ds_read_b128 v[32:35], v84 offset:7168
	v_mfma_f32_32x32x16_f16 a[48:63], v[36:39], v[112:115], a[48:63]
	s_add_u32 m0, s47, 0x103c0
	s_add_u32 s42, s42, 0x1800
	s_addc_u32 s43, s43, 0
	global_load_lds_dwordx4 v77, s[42:43]
	ds_read_b128 v[36:39], v84 offset:8192
	s_nop 0
	v_mfma_f32_32x32x16_f16 a[32:47], v[40:43], v[112:115], a[32:47]
	ds_read_b128 v[40:43], v84 offset:9216
	v_mfma_f32_32x32x16_f16 a[16:31], v[44:47], v[112:115], a[16:31]
	s_add_u32 m0, s48, 0x103c0
	s_add_u32 s44, s44, 0x1800
	s_addc_u32 s45, s45, 0
	global_load_lds_dwordx4 v78, s[44:45]
	ds_read_b128 v[44:47], v84 offset:10240
	s_nop 0
	v_mfma_f32_32x32x16_f16 a[0:15], v[48:51], v[112:115], a[0:15]
	ds_read_b128 v[48:51], v84 offset:11264
	s_waitcnt lgkmcnt(6)
	s_nop 0
	v_mfma_f32_32x32x16_f16 a[80:95], v[4:7], v[52:55], a[80:95]
	v_mfma_f32_32x32x16_f16 a[64:79], v[8:11], v[52:55], a[64:79]
	v_mfma_f32_32x32x16_f16 a[48:63], v[12:15], v[52:55], a[48:63]
	s_waitcnt vmcnt(10)
	s_waitcnt lgkmcnt(0)
	s_barrier
	ds_read_b128 v[4:7], v84 offset:12288
	ds_read_b128 v[8:11], v84 offset:13312
	ds_read_b128 v[12:15], v84 offset:14336
	s_nop 0
	v_mfma_f32_32x32x16_f16 a[32:47], v[16:19], v[52:55], a[32:47]
	ds_read_b128 v[16:19], v84 offset:15360
	v_mfma_f32_32x32x16_f16 a[16:31], v[20:23], v[52:55], a[16:31]
	ds_read_b128 v[20:23], v84 offset:16384
	v_mfma_f32_32x32x16_f16 a[0:15], v[24:27], v[52:55], a[0:15]
	ds_read_b128 v[24:27], v84 offset:17408
	v_mfma_f32_32x32x16_f16 a[80:95], v[28:31], v[56:59], a[80:95]
	s_add_u32 m0, s46, 0x0
	s_add_u32 s40, s40, 0x1800
	s_addc_u32 s41, s41, 0
	global_load_lds_dwordx4 v76, s[40:41]
	ds_read_b128 v[28:31], v84 offset:18432
	v_mfma_f32_32x32x16_f16 a[64:79], v[32:35], v[56:59], a[64:79]
	ds_read_b128 v[32:35], v84 offset:19456
	v_mfma_f32_32x32x16_f16 a[48:63], v[36:39], v[56:59], a[48:63]
	s_add_u32 m0, s47, 0x0
	s_add_u32 s42, s42, 0x1800
	s_addc_u32 s43, s43, 0
	global_load_lds_dwordx4 v77, s[42:43]
	ds_read_b128 v[36:39], v84 offset:20480
	v_mfma_f32_32x32x16_f16 a[32:47], v[40:43], v[56:59], a[32:47]
	ds_read_b128 v[40:43], v84 offset:21504
	v_mfma_f32_32x32x16_f16 a[16:31], v[44:47], v[56:59], a[16:31]
	s_add_u32 m0, s48, 0x0
	s_add_u32 s44, s44, 0x1800
	s_addc_u32 s45, s45, 0
	global_load_lds_dwordx4 v78, s[44:45]
	ds_read_b128 v[44:47], v84 offset:22528
	v_mfma_f32_32x32x16_f16 a[0:15], v[48:51], v[56:59], a[0:15]
	ds_read_b128 v[48:51], v84 offset:23552
	s_waitcnt lgkmcnt(6)
	s_nop 0
	v_mfma_f32_32x32x16_f16 a[80:95], v[4:7], v[60:63], a[80:95]
	s_waitcnt vmcnt(23)
	ds_write_b128 v81, v[116:119]
	ds_write_b128 v81, v[120:123] offset:1024
	ds_write_b128 v81, v[124:127] offset:2048
	ds_write_b128 v81, v[128:131] offset:3072
	s_nop 0
	v_mfma_f32_32x32x16_f16 a[64:79], v[8:11], v[60:63], a[64:79]
	ds_read_b128 v[100:103], v95
	ds_read_b128 v[104:107], v96
	ds_read_b128 v[108:111], v97
	ds_read_b128 v[112:115], v94
	v_mfma_f32_32x32x16_f16 a[48:63], v[12:15], v[60:63], a[48:63]
	global_load_dwordx4 v[116:119], v64, s[4:5] offset:768
	global_load_dwordx4 v[120:123], v66, s[4:5] offset:768
	global_load_dwordx4 v[124:127], v68, s[4:5] offset:768
	global_load_dwordx4 v[128:131], v70, s[4:5] offset:768
	s_waitcnt vmcnt(14)
	s_waitcnt lgkmcnt(8)
	s_barrier
	ds_read_b128 v[4:7], v84 offset:54208
	ds_read_b128 v[8:11], v84 offset:55232
	ds_read_b128 v[12:15], v84 offset:56256
	s_nop 0
	v_mfma_f32_32x32x16_f16 a[32:47], v[16:19], v[60:63], a[32:47]
	ds_read_b128 v[16:19], v84 offset:57280
	v_mfma_f32_32x32x16_f16 a[16:31], v[20:23], v[60:63], a[16:31]
	ds_read_b128 v[20:23], v84 offset:58304
	v_mfma_f32_32x32x16_f16 a[0:15], v[24:27], v[60:63], a[0:15]
	ds_read_b128 v[24:27], v84 offset:59328
	s_waitcnt lgkmcnt(6)
	s_nop 0
	v_mfma_f32_32x32x16_f16 a[80:95], v[28:31], v[0:3], a[80:95]
	s_add_u32 m0, s46, 0x3000
	s_add_u32 s40, s40, 0x1800
	s_addc_u32 s41, s41, 0
	global_load_lds_dwordx4 v76, s[40:41]
	ds_read_b128 v[28:31], v84 offset:60352
	s_nop 0
	v_mfma_f32_32x32x16_f16 a[64:79], v[32:35], v[0:3], a[64:79]
	ds_read_b128 v[32:35], v84 offset:61376
	v_mfma_f32_32x32x16_f16 a[48:63], v[36:39], v[0:3], a[48:63]
	s_add_u32 m0, s47, 0x3000
	s_add_u32 s42, s42, 0x1800
	s_addc_u32 s43, s43, 0
	global_load_lds_dwordx4 v77, s[42:43]
	ds_read_b128 v[36:39], v84 offset:62400
	s_nop 0
	v_mfma_f32_32x32x16_f16 a[32:47], v[40:43], v[0:3], a[32:47]
	ds_read_b128 v[40:43], v84 offset:63424
	v_mfma_f32_32x32x16_f16 a[16:31], v[44:47], v[0:3], a[16:31]
	s_add_u32 m0, s48, 0x3000
	s_add_u32 s44, s44, 0x1800
	s_addc_u32 s45, s45, 0
	global_load_lds_dwordx4 v78, s[44:45]
	ds_read_b128 v[44:47], v84 offset:64448
	s_nop 0
	v_mfma_f32_32x32x16_f16 a[0:15], v[48:51], v[0:3], a[0:15]
	ds_read_b128 v[48:51], v84 offset:65472
	s_waitcnt lgkmcnt(6)
	s_nop 0
	v_mfma_f32_32x32x16_f16 a[80:95], v[4:7], v[100:103], a[80:95]
	v_mfma_f32_32x32x16_f16 a[64:79], v[8:11], v[100:103], a[64:79]
	v_mfma_f32_32x32x16_f16 a[48:63], v[12:15], v[100:103], a[48:63]
	s_waitcnt vmcnt(10)
	s_waitcnt lgkmcnt(0)
	s_barrier
	ds_read_b128 v[4:7], v98
	ds_read_b128 v[8:11], v98 offset:1024
	ds_read_b128 v[12:15], v98 offset:2048
	s_nop 0
	v_mfma_f32_32x32x16_f16 a[32:47], v[16:19], v[100:103], a[32:47]
	ds_read_b128 v[16:19], v98 offset:3072
	v_mfma_f32_32x32x16_f16 a[16:31], v[20:23], v[100:103], a[16:31]
	ds_read_b128 v[20:23], v98 offset:4096
	v_mfma_f32_32x32x16_f16 a[0:15], v[24:27], v[100:103], a[0:15]
	ds_read_b128 v[24:27], v98 offset:5120
	v_mfma_f32_32x32x16_f16 a[80:95], v[28:31], v[104:107], a[80:95]
	s_add_u32 m0, s46, 0xd3c0
	s_add_u32 s40, s40, 0x1800
	s_addc_u32 s41, s41, 0
	global_load_lds_dwordx4 v76, s[40:41]
	ds_read_b128 v[28:31], v98 offset:6144
	s_nop 0
	v_mfma_f32_32x32x16_f16 a[64:79], v[32:35], v[104:107], a[64:79]
	ds_read_b128 v[32:35], v98 offset:7168
	v_mfma_f32_32x32x16_f16 a[48:63], v[36:39], v[104:107], a[48:63]
	s_add_u32 m0, s47, 0xd3c0
	s_add_u32 s42, s42, 0x1800
	s_addc_u32 s43, s43, 0
	global_load_lds_dwordx4 v77, s[42:43]
	ds_read_b128 v[36:39], v98 offset:8192
	s_nop 0
	v_mfma_f32_32x32x16_f16 a[32:47], v[40:43], v[104:107], a[32:47]
	ds_read_b128 v[40:43], v98 offset:9216
	v_mfma_f32_32x32x16_f16 a[16:31], v[44:47], v[104:107], a[16:31]
	s_add_u32 m0, s48, 0xd3c0
	s_add_u32 s44, s44, 0x1800
	s_addc_u32 s45, s45, 0
	global_load_lds_dwordx4 v78, s[44:45]
	ds_read_b128 v[44:47], v98 offset:10240
	s_nop 0
	v_mfma_f32_32x32x16_f16 a[0:15], v[48:51], v[104:107], a[0:15]
	ds_read_b128 v[48:51], v98 offset:11264
	s_waitcnt lgkmcnt(6)
	s_nop 0
	v_mfma_f32_32x32x16_f16 a[80:95], v[4:7], v[108:111], a[80:95]
	s_waitcnt vmcnt(26)
	ds_write_b128 v81, v[132:135]
	ds_write_b128 v81, v[136:139] offset:1024
	ds_write_b128 v81, v[140:143] offset:2048
	ds_write_b128 v81, v[144:147] offset:3072
	s_nop 0
	v_mfma_f32_32x32x16_f16 a[64:79], v[8:11], v[108:111], a[64:79]
	ds_read_b128 v[52:55], v95
	ds_read_b128 v[56:59], v96
	ds_read_b128 v[60:63], v97
	ds_read_b128 v[0:3], v94
	v_mfma_f32_32x32x16_f16 a[48:63], v[12:15], v[108:111], a[48:63]
	global_load_dwordx4 v[132:135], v64, s[4:5] offset:896
	global_load_dwordx4 v[136:139], v66, s[4:5] offset:896
	global_load_dwordx4 v[140:143], v68, s[4:5] offset:896
	global_load_dwordx4 v[144:147], v70, s[4:5] offset:896
	s_waitcnt vmcnt(14)
	s_waitcnt lgkmcnt(8)
	s_barrier
	ds_read_b128 v[4:7], v84 offset:0
	ds_read_b128 v[8:11], v84 offset:1024
	ds_read_b128 v[12:15], v84 offset:2048
	s_nop 0
	v_mfma_f32_32x32x16_f16 a[32:47], v[16:19], v[108:111], a[32:47]
	ds_read_b128 v[16:19], v84 offset:3072
	v_mfma_f32_32x32x16_f16 a[16:31], v[20:23], v[108:111], a[16:31]
	ds_read_b128 v[20:23], v84 offset:4096
	v_mfma_f32_32x32x16_f16 a[0:15], v[24:27], v[108:111], a[0:15]
	ds_read_b128 v[24:27], v84 offset:5120
	s_waitcnt lgkmcnt(6)
	s_nop 0
	v_mfma_f32_32x32x16_f16 a[80:95], v[28:31], v[112:115], a[80:95]
	s_add_u32 m0, s46, 0x103c0
	s_add_u32 s40, s40, 0x1800
	s_addc_u32 s41, s41, 0
	global_load_lds_dwordx4 v76, s[40:41]
	ds_read_b128 v[28:31], v84 offset:6144
	s_nop 0
	v_mfma_f32_32x32x16_f16 a[64:79], v[32:35], v[112:115], a[64:79]
	ds_read_b128 v[32:35], v84 offset:7168
	v_mfma_f32_32x32x16_f16 a[48:63], v[36:39], v[112:115], a[48:63]
	s_add_u32 m0, s47, 0x103c0
	s_add_u32 s42, s42, 0x1800
	s_addc_u32 s43, s43, 0
	global_load_lds_dwordx4 v77, s[42:43]
	ds_read_b128 v[36:39], v84 offset:8192
	s_nop 0
	v_mfma_f32_32x32x16_f16 a[32:47], v[40:43], v[112:115], a[32:47]
	ds_read_b128 v[40:43], v84 offset:9216
	v_mfma_f32_32x32x16_f16 a[16:31], v[44:47], v[112:115], a[16:31]
	s_add_u32 m0, s48, 0x103c0
	s_add_u32 s44, s44, 0x1800
	s_addc_u32 s45, s45, 0
	global_load_lds_dwordx4 v78, s[44:45]
	ds_read_b128 v[44:47], v84 offset:10240
	s_nop 0
	v_mfma_f32_32x32x16_f16 a[0:15], v[48:51], v[112:115], a[0:15]
	ds_read_b128 v[48:51], v84 offset:11264
	s_waitcnt lgkmcnt(6)
	s_nop 0
	v_mfma_f32_32x32x16_f16 a[80:95], v[4:7], v[52:55], a[80:95]
	v_mfma_f32_32x32x16_f16 a[64:79], v[8:11], v[52:55], a[64:79]
	v_mfma_f32_32x32x16_f16 a[48:63], v[12:15], v[52:55], a[48:63]
	s_waitcnt vmcnt(10)
	s_waitcnt lgkmcnt(0)
	s_barrier
	ds_read_b128 v[4:7], v84 offset:12288
	ds_read_b128 v[8:11], v84 offset:13312
	ds_read_b128 v[12:15], v84 offset:14336
	s_nop 0
	v_mfma_f32_32x32x16_f16 a[32:47], v[16:19], v[52:55], a[32:47]
	ds_read_b128 v[16:19], v84 offset:15360
	v_mfma_f32_32x32x16_f16 a[16:31], v[20:23], v[52:55], a[16:31]
	ds_read_b128 v[20:23], v84 offset:16384
	v_mfma_f32_32x32x16_f16 a[0:15], v[24:27], v[52:55], a[0:15]
	ds_read_b128 v[24:27], v84 offset:17408
	v_mfma_f32_32x32x16_f16 a[80:95], v[28:31], v[56:59], a[80:95]
	s_add_u32 m0, s46, 0x0
	s_add_u32 s40, s40, 0x1800
	s_addc_u32 s41, s41, 0
	global_load_lds_dwordx4 v76, s[40:41]
	ds_read_b128 v[28:31], v84 offset:18432
	v_mfma_f32_32x32x16_f16 a[64:79], v[32:35], v[56:59], a[64:79]
	ds_read_b128 v[32:35], v84 offset:19456
	v_mfma_f32_32x32x16_f16 a[48:63], v[36:39], v[56:59], a[48:63]
	s_add_u32 m0, s47, 0x0
	s_add_u32 s42, s42, 0x1800
	s_addc_u32 s43, s43, 0
	global_load_lds_dwordx4 v77, s[42:43]
	ds_read_b128 v[36:39], v84 offset:20480
	v_mfma_f32_32x32x16_f16 a[32:47], v[40:43], v[56:59], a[32:47]
	ds_read_b128 v[40:43], v84 offset:21504
	v_mfma_f32_32x32x16_f16 a[16:31], v[44:47], v[56:59], a[16:31]
	s_add_u32 m0, s48, 0x0
	s_add_u32 s44, s44, 0x1800
	s_addc_u32 s45, s45, 0
	global_load_lds_dwordx4 v78, s[44:45]
	ds_read_b128 v[44:47], v84 offset:22528
	v_mfma_f32_32x32x16_f16 a[0:15], v[48:51], v[56:59], a[0:15]
	ds_read_b128 v[48:51], v84 offset:23552
	s_waitcnt lgkmcnt(6)
	s_nop 0
	v_mfma_f32_32x32x16_f16 a[80:95], v[4:7], v[60:63], a[80:95]
	s_waitcnt vmcnt(26)
	ds_write_b128 v81, v[148:151]
	ds_write_b128 v81, v[152:155] offset:1024
	ds_write_b128 v81, v[156:159] offset:2048
	ds_write_b128 v81, v[72:75] offset:3072
	s_nop 0
	v_mfma_f32_32x32x16_f16 a[64:79], v[8:11], v[60:63], a[64:79]
	ds_read_b128 v[100:103], v95
	ds_read_b128 v[104:107], v96
	ds_read_b128 v[108:111], v97
	ds_read_b128 v[112:115], v94
	v_mfma_f32_32x32x16_f16 a[48:63], v[12:15], v[60:63], a[48:63]
	global_load_dwordx4 v[148:151], v64, s[4:5] offset:1024
	global_load_dwordx4 v[152:155], v66, s[4:5] offset:1024
	global_load_dwordx4 v[156:159], v68, s[4:5] offset:1024
	global_load_dwordx4 v[72:75], v70, s[4:5] offset:1024
	s_waitcnt vmcnt(14)
	s_waitcnt lgkmcnt(8)
	s_barrier
	ds_read_b128 v[4:7], v84 offset:54208
	ds_read_b128 v[8:11], v84 offset:55232
	ds_read_b128 v[12:15], v84 offset:56256
	s_nop 0
	v_mfma_f32_32x32x16_f16 a[32:47], v[16:19], v[60:63], a[32:47]
	ds_read_b128 v[16:19], v84 offset:57280
	v_mfma_f32_32x32x16_f16 a[16:31], v[20:23], v[60:63], a[16:31]
	ds_read_b128 v[20:23], v84 offset:58304
	v_mfma_f32_32x32x16_f16 a[0:15], v[24:27], v[60:63], a[0:15]
	ds_read_b128 v[24:27], v84 offset:59328
	s_waitcnt lgkmcnt(6)
	s_nop 0
	v_mfma_f32_32x32x16_f16 a[80:95], v[28:31], v[0:3], a[80:95]
	s_add_u32 m0, s46, 0x3000
	s_add_u32 s40, s40, 0x1800
	s_addc_u32 s41, s41, 0
	global_load_lds_dwordx4 v76, s[40:41]
	ds_read_b128 v[28:31], v84 offset:60352
	s_nop 0
	v_mfma_f32_32x32x16_f16 a[64:79], v[32:35], v[0:3], a[64:79]
	ds_read_b128 v[32:35], v84 offset:61376
	v_mfma_f32_32x32x16_f16 a[48:63], v[36:39], v[0:3], a[48:63]
	s_add_u32 m0, s47, 0x3000
	s_add_u32 s42, s42, 0x1800
	s_addc_u32 s43, s43, 0
	global_load_lds_dwordx4 v77, s[42:43]
	ds_read_b128 v[36:39], v84 offset:62400
	s_nop 0
	v_mfma_f32_32x32x16_f16 a[32:47], v[40:43], v[0:3], a[32:47]
	ds_read_b128 v[40:43], v84 offset:63424
	v_mfma_f32_32x32x16_f16 a[16:31], v[44:47], v[0:3], a[16:31]
	s_add_u32 m0, s48, 0x3000
	s_add_u32 s44, s44, 0x1800
	s_addc_u32 s45, s45, 0
	global_load_lds_dwordx4 v78, s[44:45]
	ds_read_b128 v[44:47], v84 offset:64448
	s_nop 0
	v_mfma_f32_32x32x16_f16 a[0:15], v[48:51], v[0:3], a[0:15]
	ds_read_b128 v[48:51], v84 offset:65472
	s_waitcnt lgkmcnt(6)
	s_nop 0
	v_mfma_f32_32x32x16_f16 a[80:95], v[4:7], v[100:103], a[80:95]
	v_mfma_f32_32x32x16_f16 a[64:79], v[8:11], v[100:103], a[64:79]
	v_mfma_f32_32x32x16_f16 a[48:63], v[12:15], v[100:103], a[48:63]
	s_waitcnt vmcnt(10)
	s_waitcnt lgkmcnt(0)
	s_barrier
	ds_read_b128 v[4:7], v98
	ds_read_b128 v[8:11], v98 offset:1024
	ds_read_b128 v[12:15], v98 offset:2048
	s_nop 0
	v_mfma_f32_32x32x16_f16 a[32:47], v[16:19], v[100:103], a[32:47]
	ds_read_b128 v[16:19], v98 offset:3072
	v_mfma_f32_32x32x16_f16 a[16:31], v[20:23], v[100:103], a[16:31]
	ds_read_b128 v[20:23], v98 offset:4096
	v_mfma_f32_32x32x16_f16 a[0:15], v[24:27], v[100:103], a[0:15]
	ds_read_b128 v[24:27], v98 offset:5120
	v_mfma_f32_32x32x16_f16 a[80:95], v[28:31], v[104:107], a[80:95]
	s_add_u32 m0, s46, 0xd3c0
	s_add_u32 s40, s40, 0x1800
	s_addc_u32 s41, s41, 0
	global_load_lds_dwordx4 v76, s[40:41]
	ds_read_b128 v[28:31], v98 offset:6144
	s_nop 0
	v_mfma_f32_32x32x16_f16 a[64:79], v[32:35], v[104:107], a[64:79]
	ds_read_b128 v[32:35], v98 offset:7168
	v_mfma_f32_32x32x16_f16 a[48:63], v[36:39], v[104:107], a[48:63]
	s_add_u32 m0, s47, 0xd3c0
	s_add_u32 s42, s42, 0x1800
	s_addc_u32 s43, s43, 0
	global_load_lds_dwordx4 v77, s[42:43]
	ds_read_b128 v[36:39], v98 offset:8192
	s_nop 0
	v_mfma_f32_32x32x16_f16 a[32:47], v[40:43], v[104:107], a[32:47]
	ds_read_b128 v[40:43], v98 offset:9216
	v_mfma_f32_32x32x16_f16 a[16:31], v[44:47], v[104:107], a[16:31]
	s_add_u32 m0, s48, 0xd3c0
	s_add_u32 s44, s44, 0x1800
	s_addc_u32 s45, s45, 0
	global_load_lds_dwordx4 v78, s[44:45]
	ds_read_b128 v[44:47], v98 offset:10240
	s_nop 0
	v_mfma_f32_32x32x16_f16 a[0:15], v[48:51], v[104:107], a[0:15]
	ds_read_b128 v[48:51], v98 offset:11264
	s_waitcnt lgkmcnt(6)
	s_nop 0
	v_mfma_f32_32x32x16_f16 a[80:95], v[4:7], v[108:111], a[80:95]
	s_waitcnt vmcnt(26)
	ds_write_b128 v81, v[116:119]
	ds_write_b128 v81, v[120:123] offset:1024
	ds_write_b128 v81, v[124:127] offset:2048
	ds_write_b128 v81, v[128:131] offset:3072
	s_nop 0
	v_mfma_f32_32x32x16_f16 a[64:79], v[8:11], v[108:111], a[64:79]
	ds_read_b128 v[52:55], v95
	ds_read_b128 v[56:59], v96
	ds_read_b128 v[60:63], v97
	ds_read_b128 v[0:3], v94
	v_mfma_f32_32x32x16_f16 a[48:63], v[12:15], v[108:111], a[48:63]
	global_load_dwordx4 v[116:119], v64, s[4:5] offset:1152
	global_load_dwordx4 v[120:123], v66, s[4:5] offset:1152
	global_load_dwordx4 v[124:127], v68, s[4:5] offset:1152
	global_load_dwordx4 v[128:131], v70, s[4:5] offset:1152
	s_waitcnt vmcnt(14)
	s_waitcnt lgkmcnt(8)
	s_barrier
	ds_read_b128 v[4:7], v84 offset:0
	ds_read_b128 v[8:11], v84 offset:1024
	ds_read_b128 v[12:15], v84 offset:2048
	s_nop 0
	v_mfma_f32_32x32x16_f16 a[32:47], v[16:19], v[108:111], a[32:47]
	ds_read_b128 v[16:19], v84 offset:3072
	v_mfma_f32_32x32x16_f16 a[16:31], v[20:23], v[108:111], a[16:31]
	ds_read_b128 v[20:23], v84 offset:4096
	v_mfma_f32_32x32x16_f16 a[0:15], v[24:27], v[108:111], a[0:15]
	ds_read_b128 v[24:27], v84 offset:5120
	s_waitcnt lgkmcnt(6)
	s_nop 0
	v_mfma_f32_32x32x16_f16 a[80:95], v[28:31], v[112:115], a[80:95]
	s_add_u32 m0, s46, 0x103c0
	s_add_u32 s40, s40, 0x1800
	s_addc_u32 s41, s41, 0
	global_load_lds_dwordx4 v76, s[40:41]
	ds_read_b128 v[28:31], v84 offset:6144
	s_nop 0
	v_mfma_f32_32x32x16_f16 a[64:79], v[32:35], v[112:115], a[64:79]
	ds_read_b128 v[32:35], v84 offset:7168
	v_mfma_f32_32x32x16_f16 a[48:63], v[36:39], v[112:115], a[48:63]
	s_add_u32 m0, s47, 0x103c0
	s_add_u32 s42, s42, 0x1800
	s_addc_u32 s43, s43, 0
	global_load_lds_dwordx4 v77, s[42:43]
	ds_read_b128 v[36:39], v84 offset:8192
	s_nop 0
	v_mfma_f32_32x32x16_f16 a[32:47], v[40:43], v[112:115], a[32:47]
	ds_read_b128 v[40:43], v84 offset:9216
	v_mfma_f32_32x32x16_f16 a[16:31], v[44:47], v[112:115], a[16:31]
	s_add_u32 m0, s48, 0x103c0
	s_add_u32 s44, s44, 0x1800
	s_addc_u32 s45, s45, 0
	global_load_lds_dwordx4 v78, s[44:45]
	ds_read_b128 v[44:47], v84 offset:10240
	s_nop 0
	v_mfma_f32_32x32x16_f16 a[0:15], v[48:51], v[112:115], a[0:15]
	ds_read_b128 v[48:51], v84 offset:11264
	s_waitcnt lgkmcnt(6)
	s_nop 0
	v_mfma_f32_32x32x16_f16 a[80:95], v[4:7], v[52:55], a[80:95]
	v_mfma_f32_32x32x16_f16 a[64:79], v[8:11], v[52:55], a[64:79]
	v_mfma_f32_32x32x16_f16 a[48:63], v[12:15], v[52:55], a[48:63]
	s_waitcnt vmcnt(10)
	s_waitcnt lgkmcnt(0)
	s_barrier
	ds_read_b128 v[4:7], v84 offset:12288
	ds_read_b128 v[8:11], v84 offset:13312
	ds_read_b128 v[12:15], v84 offset:14336
	s_nop 0
	v_mfma_f32_32x32x16_f16 a[32:47], v[16:19], v[52:55], a[32:47]
	ds_read_b128 v[16:19], v84 offset:15360
	v_mfma_f32_32x32x16_f16 a[16:31], v[20:23], v[52:55], a[16:31]
	ds_read_b128 v[20:23], v84 offset:16384
	v_mfma_f32_32x32x16_f16 a[0:15], v[24:27], v[52:55], a[0:15]
	ds_read_b128 v[24:27], v84 offset:17408
	v_mfma_f32_32x32x16_f16 a[80:95], v[28:31], v[56:59], a[80:95]
	s_add_u32 m0, s46, 0x0
	s_add_u32 s40, s40, 0x1800
	s_addc_u32 s41, s41, 0
	global_load_lds_dwordx4 v76, s[40:41]
	ds_read_b128 v[28:31], v84 offset:18432
	v_mfma_f32_32x32x16_f16 a[64:79], v[32:35], v[56:59], a[64:79]
	ds_read_b128 v[32:35], v84 offset:19456
	v_mfma_f32_32x32x16_f16 a[48:63], v[36:39], v[56:59], a[48:63]
	s_add_u32 m0, s47, 0x0
	s_add_u32 s42, s42, 0x1800
	s_addc_u32 s43, s43, 0
	global_load_lds_dwordx4 v77, s[42:43]
	ds_read_b128 v[36:39], v84 offset:20480
	v_mfma_f32_32x32x16_f16 a[32:47], v[40:43], v[56:59], a[32:47]
	ds_read_b128 v[40:43], v84 offset:21504
	v_mfma_f32_32x32x16_f16 a[16:31], v[44:47], v[56:59], a[16:31]
	s_add_u32 m0, s48, 0x0
	s_add_u32 s44, s44, 0x1800
	s_addc_u32 s45, s45, 0
	global_load_lds_dwordx4 v78, s[44:45]
	ds_read_b128 v[44:47], v84 offset:22528
	v_mfma_f32_32x32x16_f16 a[0:15], v[48:51], v[56:59], a[0:15]
	ds_read_b128 v[48:51], v84 offset:23552
	s_waitcnt lgkmcnt(6)
	s_nop 0
	v_mfma_f32_32x32x16_f16 a[80:95], v[4:7], v[60:63], a[80:95]
	s_waitcnt vmcnt(26)
	ds_write_b128 v81, v[132:135]
	ds_write_b128 v81, v[136:139] offset:1024
	ds_write_b128 v81, v[140:143] offset:2048
	ds_write_b128 v81, v[144:147] offset:3072
	s_nop 0
	v_mfma_f32_32x32x16_f16 a[64:79], v[8:11], v[60:63], a[64:79]
	ds_read_b128 v[100:103], v95
	ds_read_b128 v[104:107], v96
	ds_read_b128 v[108:111], v97
	ds_read_b128 v[112:115], v94
	v_mfma_f32_32x32x16_f16 a[48:63], v[12:15], v[60:63], a[48:63]
	global_load_dwordx4 v[132:135], v64, s[4:5] offset:1280
	global_load_dwordx4 v[136:139], v66, s[4:5] offset:1280
	global_load_dwordx4 v[140:143], v68, s[4:5] offset:1280
	global_load_dwordx4 v[144:147], v70, s[4:5] offset:1280
	s_waitcnt vmcnt(14)
	s_waitcnt lgkmcnt(8)
	s_barrier
	ds_read_b128 v[4:7], v84 offset:54208
	ds_read_b128 v[8:11], v84 offset:55232
	ds_read_b128 v[12:15], v84 offset:56256
	s_nop 0
	v_mfma_f32_32x32x16_f16 a[32:47], v[16:19], v[60:63], a[32:47]
	ds_read_b128 v[16:19], v84 offset:57280
	v_mfma_f32_32x32x16_f16 a[16:31], v[20:23], v[60:63], a[16:31]
	ds_read_b128 v[20:23], v84 offset:58304
	v_mfma_f32_32x32x16_f16 a[0:15], v[24:27], v[60:63], a[0:15]
	ds_read_b128 v[24:27], v84 offset:59328
	s_waitcnt lgkmcnt(6)
	s_nop 0
	v_mfma_f32_32x32x16_f16 a[80:95], v[28:31], v[0:3], a[80:95]
	s_add_u32 m0, s46, 0x3000
	s_add_u32 s40, s40, 0x1800
	s_addc_u32 s41, s41, 0
	global_load_lds_dwordx4 v76, s[40:41]
	ds_read_b128 v[28:31], v84 offset:60352
	s_nop 0
	v_mfma_f32_32x32x16_f16 a[64:79], v[32:35], v[0:3], a[64:79]
	ds_read_b128 v[32:35], v84 offset:61376
	v_mfma_f32_32x32x16_f16 a[48:63], v[36:39], v[0:3], a[48:63]
	s_add_u32 m0, s47, 0x3000
	s_add_u32 s42, s42, 0x1800
	s_addc_u32 s43, s43, 0
	global_load_lds_dwordx4 v77, s[42:43]
	ds_read_b128 v[36:39], v84 offset:62400
	s_nop 0
	v_mfma_f32_32x32x16_f16 a[32:47], v[40:43], v[0:3], a[32:47]
	ds_read_b128 v[40:43], v84 offset:63424
	v_mfma_f32_32x32x16_f16 a[16:31], v[44:47], v[0:3], a[16:31]
	s_add_u32 m0, s48, 0x3000
	s_add_u32 s44, s44, 0x1800
	s_addc_u32 s45, s45, 0
	global_load_lds_dwordx4 v78, s[44:45]
	ds_read_b128 v[44:47], v84 offset:64448
	s_nop 0
	v_mfma_f32_32x32x16_f16 a[0:15], v[48:51], v[0:3], a[0:15]
	ds_read_b128 v[48:51], v84 offset:65472
	s_waitcnt lgkmcnt(6)
	s_nop 0
	v_mfma_f32_32x32x16_f16 a[80:95], v[4:7], v[100:103], a[80:95]
	v_mfma_f32_32x32x16_f16 a[64:79], v[8:11], v[100:103], a[64:79]
	v_mfma_f32_32x32x16_f16 a[48:63], v[12:15], v[100:103], a[48:63]
	s_waitcnt vmcnt(10)
	s_waitcnt lgkmcnt(0)
	s_barrier
	ds_read_b128 v[4:7], v98
	ds_read_b128 v[8:11], v98 offset:1024
	ds_read_b128 v[12:15], v98 offset:2048
	s_nop 0
	v_mfma_f32_32x32x16_f16 a[32:47], v[16:19], v[100:103], a[32:47]
	ds_read_b128 v[16:19], v98 offset:3072
	v_mfma_f32_32x32x16_f16 a[16:31], v[20:23], v[100:103], a[16:31]
	ds_read_b128 v[20:23], v98 offset:4096
	v_mfma_f32_32x32x16_f16 a[0:15], v[24:27], v[100:103], a[0:15]
	ds_read_b128 v[24:27], v98 offset:5120
	v_mfma_f32_32x32x16_f16 a[80:95], v[28:31], v[104:107], a[80:95]
	s_add_u32 m0, s46, 0xd3c0
	s_add_u32 s40, s40, 0x1800
	s_addc_u32 s41, s41, 0
	global_load_lds_dwordx4 v76, s[40:41]
	ds_read_b128 v[28:31], v98 offset:6144
	s_nop 0
	v_mfma_f32_32x32x16_f16 a[64:79], v[32:35], v[104:107], a[64:79]
	ds_read_b128 v[32:35], v98 offset:7168
	v_mfma_f32_32x32x16_f16 a[48:63], v[36:39], v[104:107], a[48:63]
	s_add_u32 m0, s47, 0xd3c0
	s_add_u32 s42, s42, 0x1800
	s_addc_u32 s43, s43, 0
	global_load_lds_dwordx4 v77, s[42:43]
	ds_read_b128 v[36:39], v98 offset:8192
	s_nop 0
	v_mfma_f32_32x32x16_f16 a[32:47], v[40:43], v[104:107], a[32:47]
	ds_read_b128 v[40:43], v98 offset:9216
	v_mfma_f32_32x32x16_f16 a[16:31], v[44:47], v[104:107], a[16:31]
	s_add_u32 m0, s48, 0xd3c0
	s_add_u32 s44, s44, 0x1800
	s_addc_u32 s45, s45, 0
	global_load_lds_dwordx4 v78, s[44:45]
	ds_read_b128 v[44:47], v98 offset:10240
	s_nop 0
	v_mfma_f32_32x32x16_f16 a[0:15], v[48:51], v[104:107], a[0:15]
	ds_read_b128 v[48:51], v98 offset:11264
	s_waitcnt lgkmcnt(6)
	s_nop 0
	v_mfma_f32_32x32x16_f16 a[80:95], v[4:7], v[108:111], a[80:95]
	s_waitcnt vmcnt(26)
	ds_write_b128 v81, v[148:151]
	ds_write_b128 v81, v[152:155] offset:1024
	ds_write_b128 v81, v[156:159] offset:2048
	ds_write_b128 v81, v[72:75] offset:3072
	s_nop 0
	v_mfma_f32_32x32x16_f16 a[64:79], v[8:11], v[108:111], a[64:79]
	ds_read_b128 v[52:55], v95
	ds_read_b128 v[56:59], v96
	ds_read_b128 v[60:63], v97
	ds_read_b128 v[0:3], v94
	v_mfma_f32_32x32x16_f16 a[48:63], v[12:15], v[108:111], a[48:63]
	global_load_dwordx4 v[148:151], v64, s[4:5] offset:1408
	global_load_dwordx4 v[152:155], v66, s[4:5] offset:1408
	global_load_dwordx4 v[156:159], v68, s[4:5] offset:1408
	global_load_dwordx4 v[72:75], v70, s[4:5] offset:1408
	s_waitcnt vmcnt(14)
	s_waitcnt lgkmcnt(8)
	s_barrier
	ds_read_b128 v[4:7], v84 offset:0
	ds_read_b128 v[8:11], v84 offset:1024
	ds_read_b128 v[12:15], v84 offset:2048
	s_nop 0
	v_mfma_f32_32x32x16_f16 a[32:47], v[16:19], v[108:111], a[32:47]
	ds_read_b128 v[16:19], v84 offset:3072
	v_mfma_f32_32x32x16_f16 a[16:31], v[20:23], v[108:111], a[16:31]
	ds_read_b128 v[20:23], v84 offset:4096
	v_mfma_f32_32x32x16_f16 a[0:15], v[24:27], v[108:111], a[0:15]
	ds_read_b128 v[24:27], v84 offset:5120
	s_waitcnt lgkmcnt(6)
	s_nop 0
	v_mfma_f32_32x32x16_f16 a[80:95], v[28:31], v[112:115], a[80:95]
	s_add_u32 m0, s46, 0x103c0
	s_add_u32 s40, s40, 0x1800
	s_addc_u32 s41, s41, 0
	global_load_lds_dwordx4 v76, s[40:41]
	ds_read_b128 v[28:31], v84 offset:6144
	s_nop 0
	v_mfma_f32_32x32x16_f16 a[64:79], v[32:35], v[112:115], a[64:79]
	ds_read_b128 v[32:35], v84 offset:7168
	v_mfma_f32_32x32x16_f16 a[48:63], v[36:39], v[112:115], a[48:63]
	s_add_u32 m0, s47, 0x103c0
	s_add_u32 s42, s42, 0x1800
	s_addc_u32 s43, s43, 0
	global_load_lds_dwordx4 v77, s[42:43]
	ds_read_b128 v[36:39], v84 offset:8192
	s_nop 0
	v_mfma_f32_32x32x16_f16 a[32:47], v[40:43], v[112:115], a[32:47]
	ds_read_b128 v[40:43], v84 offset:9216
	v_mfma_f32_32x32x16_f16 a[16:31], v[44:47], v[112:115], a[16:31]
	s_add_u32 m0, s48, 0x103c0
	s_add_u32 s44, s44, 0x1800
	s_addc_u32 s45, s45, 0
	global_load_lds_dwordx4 v78, s[44:45]
	ds_read_b128 v[44:47], v84 offset:10240
	s_nop 0
	v_mfma_f32_32x32x16_f16 a[0:15], v[48:51], v[112:115], a[0:15]
	ds_read_b128 v[48:51], v84 offset:11264
	s_waitcnt lgkmcnt(6)
	s_nop 0
	v_mfma_f32_32x32x16_f16 a[80:95], v[4:7], v[52:55], a[80:95]
	v_mfma_f32_32x32x16_f16 a[64:79], v[8:11], v[52:55], a[64:79]
	v_mfma_f32_32x32x16_f16 a[48:63], v[12:15], v[52:55], a[48:63]
	s_waitcnt vmcnt(10)
	s_waitcnt lgkmcnt(0)
	s_barrier
	ds_read_b128 v[4:7], v84 offset:12288
	ds_read_b128 v[8:11], v84 offset:13312
	ds_read_b128 v[12:15], v84 offset:14336
	s_nop 0
	v_mfma_f32_32x32x16_f16 a[32:47], v[16:19], v[52:55], a[32:47]
	ds_read_b128 v[16:19], v84 offset:15360
	v_mfma_f32_32x32x16_f16 a[16:31], v[20:23], v[52:55], a[16:31]
	ds_read_b128 v[20:23], v84 offset:16384
	v_mfma_f32_32x32x16_f16 a[0:15], v[24:27], v[52:55], a[0:15]
	ds_read_b128 v[24:27], v84 offset:17408
	v_mfma_f32_32x32x16_f16 a[80:95], v[28:31], v[56:59], a[80:95]
	s_add_u32 m0, s46, 0x0
	s_add_u32 s40, s40, 0x1800
	s_addc_u32 s41, s41, 0
	global_load_lds_dwordx4 v76, s[40:41]
	ds_read_b128 v[28:31], v84 offset:18432
	v_mfma_f32_32x32x16_f16 a[64:79], v[32:35], v[56:59], a[64:79]
	ds_read_b128 v[32:35], v84 offset:19456
	v_mfma_f32_32x32x16_f16 a[48:63], v[36:39], v[56:59], a[48:63]
	s_add_u32 m0, s47, 0x0
	s_add_u32 s42, s42, 0x1800
	s_addc_u32 s43, s43, 0
	global_load_lds_dwordx4 v77, s[42:43]
	ds_read_b128 v[36:39], v84 offset:20480
	v_mfma_f32_32x32x16_f16 a[32:47], v[40:43], v[56:59], a[32:47]
	ds_read_b128 v[40:43], v84 offset:21504
	v_mfma_f32_32x32x16_f16 a[16:31], v[44:47], v[56:59], a[16:31]
	s_add_u32 m0, s48, 0x0
	s_add_u32 s44, s44, 0x1800
	s_addc_u32 s45, s45, 0
	global_load_lds_dwordx4 v78, s[44:45]
	ds_read_b128 v[44:47], v84 offset:22528
	v_mfma_f32_32x32x16_f16 a[0:15], v[48:51], v[56:59], a[0:15]
	ds_read_b128 v[48:51], v84 offset:23552
	s_waitcnt lgkmcnt(6)
	s_nop 0
	v_mfma_f32_32x32x16_f16 a[80:95], v[4:7], v[60:63], a[80:95]
	s_waitcnt vmcnt(26)
	ds_write_b128 v81, v[116:119]
	ds_write_b128 v81, v[120:123] offset:1024
	ds_write_b128 v81, v[124:127] offset:2048
	ds_write_b128 v81, v[128:131] offset:3072
	s_nop 0
	v_mfma_f32_32x32x16_f16 a[64:79], v[8:11], v[60:63], a[64:79]
	ds_read_b128 v[100:103], v95
	ds_read_b128 v[104:107], v96
	ds_read_b128 v[108:111], v97
	ds_read_b128 v[112:115], v94
	v_mfma_f32_32x32x16_f16 a[48:63], v[12:15], v[60:63], a[48:63]
	global_load_dwordx4 v[116:119], v64, s[4:5] offset:1440
	global_load_dwordx4 v[120:123], v66, s[4:5] offset:1440
	global_load_dwordx4 v[124:127], v68, s[4:5] offset:1440
	global_load_dwordx4 v[128:131], v70, s[4:5] offset:1440
	s_waitcnt vmcnt(14)
	s_waitcnt lgkmcnt(8)
	s_barrier
	ds_read_b128 v[4:7], v84 offset:54208
	ds_read_b128 v[8:11], v84 offset:55232
	ds_read_b128 v[12:15], v84 offset:56256
	s_nop 0
	v_mfma_f32_32x32x16_f16 a[32:47], v[16:19], v[60:63], a[32:47]
	ds_read_b128 v[16:19], v84 offset:57280
	v_mfma_f32_32x32x16_f16 a[16:31], v[20:23], v[60:63], a[16:31]
	ds_read_b128 v[20:23], v84 offset:58304
	v_mfma_f32_32x32x16_f16 a[0:15], v[24:27], v[60:63], a[0:15]
	ds_read_b128 v[24:27], v84 offset:59328
	s_waitcnt lgkmcnt(6)
	s_nop 0
	v_mfma_f32_32x32x16_f16 a[80:95], v[28:31], v[0:3], a[80:95]
	s_add_u32 m0, s46, 0x3000
	s_add_u32 s40, s40, 0x1800
	s_addc_u32 s41, s41, 0
	global_load_lds_dwordx4 v76, s[40:41]
	ds_read_b128 v[28:31], v84 offset:60352
	s_nop 0
	v_mfma_f32_32x32x16_f16 a[64:79], v[32:35], v[0:3], a[64:79]
	ds_read_b128 v[32:35], v84 offset:61376
	v_mfma_f32_32x32x16_f16 a[48:63], v[36:39], v[0:3], a[48:63]
	s_add_u32 m0, s47, 0x3000
	s_add_u32 s42, s42, 0x1800
	s_addc_u32 s43, s43, 0
	global_load_lds_dwordx4 v77, s[42:43]
	ds_read_b128 v[36:39], v84 offset:62400
	s_nop 0
	v_mfma_f32_32x32x16_f16 a[32:47], v[40:43], v[0:3], a[32:47]
	ds_read_b128 v[40:43], v84 offset:63424
	v_mfma_f32_32x32x16_f16 a[16:31], v[44:47], v[0:3], a[16:31]
	s_add_u32 m0, s48, 0x3000
	s_add_u32 s44, s44, 0x1800
	s_addc_u32 s45, s45, 0
	global_load_lds_dwordx4 v78, s[44:45]
	ds_read_b128 v[44:47], v84 offset:64448
	s_nop 0
	v_mfma_f32_32x32x16_f16 a[0:15], v[48:51], v[0:3], a[0:15]
	ds_read_b128 v[48:51], v84 offset:65472
	s_waitcnt lgkmcnt(6)
	s_nop 0
	v_mfma_f32_32x32x16_f16 a[80:95], v[4:7], v[100:103], a[80:95]
	v_mfma_f32_32x32x16_f16 a[64:79], v[8:11], v[100:103], a[64:79]
	v_mfma_f32_32x32x16_f16 a[48:63], v[12:15], v[100:103], a[48:63]
	s_waitcnt vmcnt(10)
	s_waitcnt lgkmcnt(0)
	s_barrier
	ds_read_b128 v[4:7], v98
	ds_read_b128 v[8:11], v98 offset:1024
	ds_read_b128 v[12:15], v98 offset:2048
	s_nop 0
	v_mfma_f32_32x32x16_f16 a[32:47], v[16:19], v[100:103], a[32:47]
	ds_read_b128 v[16:19], v98 offset:3072
	v_mfma_f32_32x32x16_f16 a[16:31], v[20:23], v[100:103], a[16:31]
	ds_read_b128 v[20:23], v98 offset:4096
	v_mfma_f32_32x32x16_f16 a[0:15], v[24:27], v[100:103], a[0:15]
	ds_read_b128 v[24:27], v98 offset:5120
	v_mfma_f32_32x32x16_f16 a[80:95], v[28:31], v[104:107], a[80:95]
	s_add_u32 m0, s46, 0xd3c0
	s_add_u32 s40, s40, 0x1800
	s_addc_u32 s41, s41, 0
	global_load_lds_dwordx4 v76, s[40:41]
	ds_read_b128 v[28:31], v98 offset:6144
	s_nop 0
	v_mfma_f32_32x32x16_f16 a[64:79], v[32:35], v[104:107], a[64:79]
	ds_read_b128 v[32:35], v98 offset:7168
	v_mfma_f32_32x32x16_f16 a[48:63], v[36:39], v[104:107], a[48:63]
	s_add_u32 m0, s47, 0xd3c0
	s_add_u32 s42, s42, 0x1800
	s_addc_u32 s43, s43, 0
	global_load_lds_dwordx4 v77, s[42:43]
	ds_read_b128 v[36:39], v98 offset:8192
	s_nop 0
	v_mfma_f32_32x32x16_f16 a[32:47], v[40:43], v[104:107], a[32:47]
	ds_read_b128 v[40:43], v98 offset:9216
	v_mfma_f32_32x32x16_f16 a[16:31], v[44:47], v[104:107], a[16:31]
	s_add_u32 m0, s48, 0xd3c0
	s_add_u32 s44, s44, 0x1800
	s_addc_u32 s45, s45, 0
	global_load_lds_dwordx4 v78, s[44:45]
	ds_read_b128 v[44:47], v98 offset:10240
	s_nop 0
	v_mfma_f32_32x32x16_f16 a[0:15], v[48:51], v[104:107], a[0:15]
	ds_read_b128 v[48:51], v98 offset:11264
	s_waitcnt lgkmcnt(6)
	s_nop 0
	v_mfma_f32_32x32x16_f16 a[80:95], v[4:7], v[108:111], a[80:95]
	s_waitcnt vmcnt(26)
	ds_write_b128 v81, v[132:135]
	ds_write_b128 v81, v[136:139] offset:1024
	ds_write_b128 v81, v[140:143] offset:2048
	ds_write_b128 v81, v[144:147] offset:3072
	s_nop 0
	v_mfma_f32_32x32x16_f16 a[64:79], v[8:11], v[108:111], a[64:79]
	ds_read_b128 v[52:55], v95
	ds_read_b128 v[56:59], v96
	ds_read_b128 v[60:63], v97
	ds_read_b128 v[0:3], v94
	v_mfma_f32_32x32x16_f16 a[48:63], v[12:15], v[108:111], a[48:63]
	s_waitcnt vmcnt(10)
	s_waitcnt lgkmcnt(8)
	s_barrier
	ds_read_b128 v[4:7], v84 offset:0
	ds_read_b128 v[8:11], v84 offset:1024
	ds_read_b128 v[12:15], v84 offset:2048
	s_nop 0
	v_mfma_f32_32x32x16_f16 a[32:47], v[16:19], v[108:111], a[32:47]
	ds_read_b128 v[16:19], v84 offset:3072
	v_mfma_f32_32x32x16_f16 a[16:31], v[20:23], v[108:111], a[16:31]
	ds_read_b128 v[20:23], v84 offset:4096
	v_mfma_f32_32x32x16_f16 a[0:15], v[24:27], v[108:111], a[0:15]
	ds_read_b128 v[24:27], v84 offset:5120
	s_waitcnt lgkmcnt(6)
	s_nop 0
	v_mfma_f32_32x32x16_f16 a[80:95], v[28:31], v[112:115], a[80:95]
	s_add_u32 m0, s46, 0x103c0
	s_add_u32 s40, s40, 0x1800
	s_addc_u32 s41, s41, 0
	global_load_lds_dwordx4 v76, s[40:41]
	ds_read_b128 v[28:31], v84 offset:6144
	s_nop 0
	v_mfma_f32_32x32x16_f16 a[64:79], v[32:35], v[112:115], a[64:79]
	ds_read_b128 v[32:35], v84 offset:7168
	v_mfma_f32_32x32x16_f16 a[48:63], v[36:39], v[112:115], a[48:63]
	s_add_u32 m0, s47, 0x103c0
	s_add_u32 s42, s42, 0x1800
	s_addc_u32 s43, s43, 0
	global_load_lds_dwordx4 v77, s[42:43]
	ds_read_b128 v[36:39], v84 offset:8192
	s_nop 0
	v_mfma_f32_32x32x16_f16 a[32:47], v[40:43], v[112:115], a[32:47]
	ds_read_b128 v[40:43], v84 offset:9216
	v_mfma_f32_32x32x16_f16 a[16:31], v[44:47], v[112:115], a[16:31]
	s_add_u32 m0, s48, 0x103c0
	s_add_u32 s44, s44, 0x1800
	s_addc_u32 s45, s45, 0
	global_load_lds_dwordx4 v78, s[44:45]
	ds_read_b128 v[44:47], v84 offset:10240
	s_nop 0
	v_mfma_f32_32x32x16_f16 a[0:15], v[48:51], v[112:115], a[0:15]
	ds_read_b128 v[48:51], v84 offset:11264
	s_waitcnt lgkmcnt(6)
	s_nop 0
	v_mfma_f32_32x32x16_f16 a[80:95], v[4:7], v[52:55], a[80:95]
	v_mfma_f32_32x32x16_f16 a[64:79], v[8:11], v[52:55], a[64:79]
	v_mfma_f32_32x32x16_f16 a[48:63], v[12:15], v[52:55], a[48:63]
	s_waitcnt vmcnt(6)
	s_waitcnt lgkmcnt(0)
	s_barrier
	ds_read_b128 v[4:7], v84 offset:12288
	ds_read_b128 v[8:11], v84 offset:13312
	ds_read_b128 v[12:15], v84 offset:14336
	s_nop 0
	v_mfma_f32_32x32x16_f16 a[32:47], v[16:19], v[52:55], a[32:47]
	ds_read_b128 v[16:19], v84 offset:15360
	v_mfma_f32_32x32x16_f16 a[16:31], v[20:23], v[52:55], a[16:31]
	ds_read_b128 v[20:23], v84 offset:16384
	v_mfma_f32_32x32x16_f16 a[0:15], v[24:27], v[52:55], a[0:15]
	ds_read_b128 v[24:27], v84 offset:17408
	v_mfma_f32_32x32x16_f16 a[80:95], v[28:31], v[56:59], a[80:95]
	s_add_u32 m0, s46, 0x0
	s_add_u32 s40, s40, 0x1800
	s_addc_u32 s41, s41, 0
	global_load_lds_dwordx4 v76, s[40:41]
	ds_read_b128 v[28:31], v84 offset:18432
	v_mfma_f32_32x32x16_f16 a[64:79], v[32:35], v[56:59], a[64:79]
	ds_read_b128 v[32:35], v84 offset:19456
	v_mfma_f32_32x32x16_f16 a[48:63], v[36:39], v[56:59], a[48:63]
	s_add_u32 m0, s47, 0x0
	s_add_u32 s42, s42, s49
	s_addc_u32 s43, s43, 0
	global_load_lds_dwordx4 v77, s[42:43]
	ds_read_b128 v[36:39], v84 offset:20480
	s_nop 0
	v_mfma_f32_32x32x16_f16 a[32:47], v[40:43], v[56:59], a[32:47]
	ds_read_b128 v[40:43], v84 offset:21504
	v_mfma_f32_32x32x16_f16 a[16:31], v[44:47], v[56:59], a[16:31]
	s_add_u32 m0, s48, 0x0
	s_add_u32 s44, s44, 0xc00
	s_addc_u32 s45, s45, 0
	global_load_lds_dwordx4 v78, s[44:45]
	ds_read_b128 v[44:47], v84 offset:22528
	v_mfma_f32_32x32x16_f16 a[0:15], v[48:51], v[56:59], a[0:15]
	ds_read_b128 v[48:51], v84 offset:23552
	s_waitcnt lgkmcnt(6)
	s_nop 0
	v_mfma_f32_32x32x16_f16 a[80:95], v[4:7], v[60:63], a[80:95]
	s_waitcnt vmcnt(22)
	ds_write_b128 v81, v[148:151]
	ds_write_b128 v81, v[152:155] offset:1024
	ds_write_b128 v81, v[156:159] offset:2048
	ds_write_b128 v81, v[72:75] offset:3072
	s_nop 0
	v_mfma_f32_32x32x16_f16 a[64:79], v[8:11], v[60:63], a[64:79]
	ds_read_b128 v[100:103], v95
	ds_read_b128 v[104:107], v96
	ds_read_b128 v[108:111], v97
	ds_read_b128 v[112:115], v94
	v_mfma_f32_32x32x16_f16 a[48:63], v[12:15], v[60:63], a[48:63]
	s_waitcnt vmcnt(6)
	s_waitcnt lgkmcnt(8)
	s_barrier
	ds_read_b128 v[4:7], v84 offset:54208
	ds_read_b128 v[8:11], v84 offset:55232
	ds_read_b128 v[12:15], v84 offset:56256
	s_nop 0
	v_mfma_f32_32x32x16_f16 a[32:47], v[16:19], v[60:63], a[32:47]
	ds_read_b128 v[16:19], v84 offset:57280
	v_mfma_f32_32x32x16_f16 a[16:31], v[20:23], v[60:63], a[16:31]
	ds_read_b128 v[20:23], v84 offset:58304
	v_mfma_f32_32x32x16_f16 a[0:15], v[24:27], v[60:63], a[0:15]
	ds_read_b128 v[24:27], v84 offset:59328
	s_waitcnt lgkmcnt(6)
	s_nop 0
	v_mfma_f32_32x32x16_f16 a[80:95], v[28:31], v[0:3], a[80:95]
	ds_read_b128 v[28:31], v84 offset:60352
	v_mfma_f32_32x32x16_f16 a[64:79], v[32:35], v[0:3], a[64:79]
	ds_read_b128 v[32:35], v84 offset:61376
	v_mfma_f32_32x32x16_f16 a[48:63], v[36:39], v[0:3], a[48:63]
	ds_read_b128 v[36:39], v84 offset:62400
	v_mfma_f32_32x32x16_f16 a[32:47], v[40:43], v[0:3], a[32:47]
	ds_read_b128 v[40:43], v84 offset:63424
	v_mfma_f32_32x32x16_f16 a[16:31], v[44:47], v[0:3], a[16:31]
	ds_read_b128 v[44:47], v84 offset:64448
	v_mfma_f32_32x32x16_f16 a[0:15], v[48:51], v[0:3], a[0:15]
	ds_read_b128 v[48:51], v84 offset:65472
	s_waitcnt lgkmcnt(6)
	s_nop 0
	v_mfma_f32_32x32x16_f16 a[80:95], v[4:7], v[100:103], a[80:95]
	v_mfma_f32_32x32x16_f16 a[64:79], v[8:11], v[100:103], a[64:79]
	v_mfma_f32_32x32x16_f16 a[48:63], v[12:15], v[100:103], a[48:63]
	s_waitcnt vmcnt(3)
	s_waitcnt lgkmcnt(0)
	s_barrier
	ds_read_b128 v[4:7], v98
	ds_read_b128 v[8:11], v98 offset:1024
	ds_read_b128 v[12:15], v98 offset:2048
	s_nop 0
	v_mfma_f32_32x32x16_f16 a[32:47], v[16:19], v[100:103], a[32:47]
	ds_read_b128 v[16:19], v98 offset:3072
	v_mfma_f32_32x32x16_f16 a[16:31], v[20:23], v[100:103], a[16:31]
	ds_read_b128 v[20:23], v98 offset:4096
	v_mfma_f32_32x32x16_f16 a[0:15], v[24:27], v[100:103], a[0:15]
	ds_read_b128 v[24:27], v98 offset:5120
	v_mfma_f32_32x32x16_f16 a[80:95], v[28:31], v[104:107], a[80:95]
	ds_read_b128 v[28:31], v98 offset:6144
	v_mfma_f32_32x32x16_f16 a[64:79], v[32:35], v[104:107], a[64:79]
	ds_read_b128 v[32:35], v98 offset:7168
	v_mfma_f32_32x32x16_f16 a[48:63], v[36:39], v[104:107], a[48:63]
	ds_read_b128 v[36:39], v98 offset:8192
	v_mfma_f32_32x32x16_f16 a[32:47], v[40:43], v[104:107], a[32:47]
	ds_read_b128 v[40:43], v98 offset:9216
	v_mfma_f32_32x32x16_f16 a[16:31], v[44:47], v[104:107], a[16:31]
	ds_read_b128 v[44:47], v98 offset:10240
	v_mfma_f32_32x32x16_f16 a[0:15], v[48:51], v[104:107], a[0:15]
	ds_read_b128 v[48:51], v98 offset:11264
	s_waitcnt lgkmcnt(6)
	s_nop 0
	v_mfma_f32_32x32x16_f16 a[80:95], v[4:7], v[108:111], a[80:95]
	s_waitcnt vmcnt(12)
	ds_write_b128 v81, v[116:119]
	ds_write_b128 v81, v[120:123] offset:1024
	ds_write_b128 v81, v[124:127] offset:2048
	ds_write_b128 v81, v[128:131] offset:3072
	s_nop 0
	v_mfma_f32_32x32x16_f16 a[64:79], v[8:11], v[108:111], a[64:79]
	ds_read_b128 v[0:3], v94
	v_mfma_f32_32x32x16_f16 a[48:63], v[12:15], v[108:111], a[48:63]
	s_waitcnt vmcnt(0)
	s_waitcnt lgkmcnt(5)
	s_barrier
	ds_read_b128 v[4:7], v84 offset:0
	ds_read_b128 v[8:11], v84 offset:1024
	ds_read_b128 v[12:15], v84 offset:2048
	s_nop 0
	v_mfma_f32_32x32x16_f16 a[32:47], v[16:19], v[108:111], a[32:47]
	ds_read_b128 v[16:19], v84 offset:3072
	v_mfma_f32_32x32x16_f16 a[16:31], v[20:23], v[108:111], a[16:31]
	ds_read_b128 v[20:23], v84 offset:4096
	v_mfma_f32_32x32x16_f16 a[0:15], v[24:27], v[108:111], a[0:15]
	ds_read_b128 v[24:27], v84 offset:5120
	s_waitcnt lgkmcnt(6)
	s_nop 0
	v_mfma_f32_32x32x16_f16 a[80:95], v[28:31], v[112:115], a[80:95]
	v_mfma_f32_32x32x16_f16 a[64:79], v[32:35], v[112:115], a[64:79]
	v_mfma_f32_32x32x16_f16 a[48:63], v[36:39], v[112:115], a[48:63]
	v_mfma_f32_32x32x16_f16 a[32:47], v[40:43], v[112:115], a[32:47]
	v_mfma_f32_32x32x16_f16 a[16:31], v[44:47], v[112:115], a[16:31]
	v_mfma_f32_32x32x16_f16 a[0:15], v[48:51], v[112:115], a[0:15]
	s_waitcnt lgkmcnt(0)
	v_mfma_f32_32x32x16_f16 a[80:95], v[4:7], v[0:3], a[80:95]
	v_mfma_f32_32x32x16_f16 a[16:31], v[20:23], v[0:3], a[16:31]
	v_lshlrev_b32_e32 v22, 4, v85
	v_mfma_f32_32x32x16_f16 a[64:79], v[8:11], v[0:3], a[64:79]
	v_mfma_f32_32x32x16_f16 a[48:63], v[12:15], v[0:3], a[48:63]
	s_nop 7
	v_accvgpr_read_b32 v13, a88
	v_mfma_f32_32x32x16_f16 a[32:47], v[16:19], v[0:3], a[32:47]
	v_accvgpr_read_b32 v17, a92
	v_mfma_f32_32x32x16_f16 a[0:15], v[24:27], v[0:3], a[0:15]
	ds_read_b128 v[2:5], v22 offset:53248
	ds_read_b128 v[6:9], v22 offset:53280
	v_accvgpr_read_b32 v1, a80
	v_lshlrev_b32_e32 v0, 4, v92
	s_waitcnt lgkmcnt(1)
	v_add_f32_e32 v1, v1, v2
	v_accvgpr_read_b32 v2, a81
	v_add_f32_e32 v2, v3, v2
	v_max_f32_e32 v10, 0, v2
	v_accvgpr_read_b32 v2, a82
	v_add_f32_e32 v2, v4, v2
	v_max_f32_e32 v11, 0, v2
	v_accvgpr_read_b32 v2, a83
	v_add_f32_e32 v2, v5, v2
	v_max_f32_e32 v12, 0, v2
	v_accvgpr_read_b32 v2, a84
	s_waitcnt lgkmcnt(0)
	v_add_f32_e32 v2, v2, v6
	v_max_f32_e32 v6, 0, v2
	v_accvgpr_read_b32 v2, a85
	v_add_f32_e32 v2, v7, v2
	v_max_f32_e32 v7, 0, v2
	v_accvgpr_read_b32 v2, a86
	v_add_f32_e32 v2, v8, v2
	v_max_f32_e32 v8, 0, v2
	v_accvgpr_read_b32 v2, a87
	v_add_f32_e32 v2, v9, v2
	v_max_f32_e32 v9, 0, v2
	ds_read_b128 v[2:5], v22 offset:53312
	v_max_f32_e32 v1, 0, v1
	s_waitcnt lgkmcnt(0)
	v_add_f32_e32 v2, v13, v2
	v_max_f32_e32 v13, 0, v2
	v_accvgpr_read_b32 v2, a89
	v_add_f32_e32 v2, v3, v2
	v_max_f32_e32 v14, 0, v2
	v_accvgpr_read_b32 v2, a90
	v_add_f32_e32 v2, v4, v2
	v_max_f32_e32 v15, 0, v2
	v_accvgpr_read_b32 v2, a91
	v_add_f32_e32 v2, v5, v2
	v_max_f32_e32 v16, 0, v2
	ds_read_b128 v[2:5], v22 offset:53344
	s_waitcnt lgkmcnt(0)
	v_add_f32_e32 v2, v17, v2
	v_max_f32_e32 v17, 0, v2
	v_accvgpr_read_b32 v2, a93
	v_add_f32_e32 v2, v3, v2
	v_max_f32_e32 v18, 0, v2
	v_accvgpr_read_b32 v2, a94
	v_add_f32_e32 v2, v4, v2
	v_max_f32_e32 v19, 0, v2
	v_accvgpr_read_b32 v2, a95
	v_add_f32_e32 v2, v5, v2
	v_cvt_pk_f16_f32 v5, v8, v9
	v_cvt_pk_f16_f32 v4, v6, v7
	ds_read_b128 v[6:9], v0 offset:40960
	v_max_f32_e32 v20, 0, v2
	v_cvt_pk_f16_f32 v3, v11, v12
	v_cvt_pk_f16_f32 v2, v1, v10
	v_accvgpr_read_b32 v1, a64
	s_waitcnt lgkmcnt(0)
	v_mfma_f32_32x32x16_f16 a[80:95], v[6:9], v[2:5], 0
	ds_read_b128 v[6:9], v0 offset:41984
	v_cvt_pk_f16_f32 v5, v19, v20
	v_cvt_pk_f16_f32 v4, v17, v18
	v_cvt_pk_f16_f32 v3, v15, v16
	v_cvt_pk_f16_f32 v2, v13, v14
	v_accvgpr_read_b32 v13, a72
	v_accvgpr_read_b32 v17, a76
	s_waitcnt lgkmcnt(0)
	v_mfma_f32_32x32x16_f16 a[80:95], v[6:9], v[2:5], a[80:95]
	ds_read_b128 v[2:5], v22 offset:53376
	v_accvgpr_read_b32 v9, a68
	s_waitcnt lgkmcnt(0)
	v_add_f32_e32 v1, v1, v2
	v_accvgpr_read_b32 v2, a65
	v_add_f32_e32 v2, v3, v2
	v_max_f32_e32 v6, 0, v2
	v_accvgpr_read_b32 v2, a66
	v_add_f32_e32 v2, v4, v2
	v_max_f32_e32 v7, 0, v2
	v_accvgpr_read_b32 v2, a67
	v_add_f32_e32 v2, v5, v2
	v_max_f32_e32 v8, 0, v2
	ds_read_b128 v[2:5], v22 offset:53408
	v_max_f32_e32 v1, 0, v1
	s_waitcnt lgkmcnt(0)
	v_add_f32_e32 v2, v9, v2
	v_max_f32_e32 v9, 0, v2
	v_accvgpr_read_b32 v2, a69
	v_add_f32_e32 v2, v3, v2
	v_max_f32_e32 v10, 0, v2
	v_accvgpr_read_b32 v2, a70
	v_add_f32_e32 v2, v4, v2
	v_max_f32_e32 v11, 0, v2
	v_accvgpr_read_b32 v2, a71
	v_add_f32_e32 v2, v5, v2
	v_max_f32_e32 v12, 0, v2
	ds_read_b128 v[2:5], v22 offset:53440
	s_waitcnt lgkmcnt(0)
	v_add_f32_e32 v2, v13, v2
	v_max_f32_e32 v13, 0, v2
	v_accvgpr_read_b32 v2, a73
	v_add_f32_e32 v2, v3, v2
	v_max_f32_e32 v14, 0, v2
	v_accvgpr_read_b32 v2, a74
	v_add_f32_e32 v2, v4, v2
	v_max_f32_e32 v15, 0, v2
	v_accvgpr_read_b32 v2, a75
	v_add_f32_e32 v2, v5, v2
	v_max_f32_e32 v16, 0, v2
	ds_read_b128 v[2:5], v22 offset:53472
	s_waitcnt lgkmcnt(0)
	v_add_f32_e32 v2, v17, v2
	v_max_f32_e32 v17, 0, v2
	v_accvgpr_read_b32 v2, a77
	v_add_f32_e32 v2, v3, v2
	v_max_f32_e32 v18, 0, v2
	v_accvgpr_read_b32 v2, a78
	v_add_f32_e32 v2, v4, v2
	v_max_f32_e32 v19, 0, v2
	v_accvgpr_read_b32 v2, a79
	v_add_f32_e32 v2, v5, v2
	v_max_f32_e32 v20, 0, v2
	v_cvt_pk_f16_f32 v4, v9, v10
	v_cvt_pk_f16_f32 v3, v7, v8
	v_cvt_pk_f16_f32 v2, v1, v6
	ds_read_b128 v[6:9], v0 offset:43008
	v_cvt_pk_f16_f32 v5, v11, v12
	v_accvgpr_read_b32 v1, a48
	s_waitcnt lgkmcnt(0)
	v_mfma_f32_32x32x16_f16 a[80:95], v[6:9], v[2:5], a[80:95]
	ds_read_b128 v[6:9], v0 offset:44032
	v_cvt_pk_f16_f32 v5, v19, v20
	v_cvt_pk_f16_f32 v4, v17, v18
	v_cvt_pk_f16_f32 v3, v15, v16
	v_cvt_pk_f16_f32 v2, v13, v14
	v_accvgpr_read_b32 v13, a56
	v_accvgpr_read_b32 v17, a60
	s_waitcnt lgkmcnt(0)
	v_mfma_f32_32x32x16_f16 a[80:95], v[6:9], v[2:5], a[80:95]
	ds_read_b128 v[2:5], v22 offset:53504
	v_accvgpr_read_b32 v9, a52
	s_waitcnt lgkmcnt(0)
	v_add_f32_e32 v1, v1, v2
	v_accvgpr_read_b32 v2, a49
	v_add_f32_e32 v2, v3, v2
	v_max_f32_e32 v6, 0, v2
	v_accvgpr_read_b32 v2, a50
	v_add_f32_e32 v2, v4, v2
	v_max_f32_e32 v7, 0, v2
	v_accvgpr_read_b32 v2, a51
	v_add_f32_e32 v2, v5, v2
	v_max_f32_e32 v8, 0, v2
	ds_read_b128 v[2:5], v22 offset:53536
	v_max_f32_e32 v1, 0, v1
	s_waitcnt lgkmcnt(0)
	v_add_f32_e32 v2, v9, v2
	v_max_f32_e32 v9, 0, v2
	v_accvgpr_read_b32 v2, a53
	v_add_f32_e32 v2, v3, v2
	v_max_f32_e32 v10, 0, v2
	v_accvgpr_read_b32 v2, a54
	v_add_f32_e32 v2, v4, v2
	v_max_f32_e32 v11, 0, v2
	v_accvgpr_read_b32 v2, a55
	v_add_f32_e32 v2, v5, v2
	v_max_f32_e32 v12, 0, v2
	ds_read_b128 v[2:5], v22 offset:53568
	s_waitcnt lgkmcnt(0)
	v_add_f32_e32 v2, v13, v2
	v_max_f32_e32 v13, 0, v2
	v_accvgpr_read_b32 v2, a57
	v_add_f32_e32 v2, v3, v2
	v_max_f32_e32 v14, 0, v2
	v_accvgpr_read_b32 v2, a58
	v_add_f32_e32 v2, v4, v2
	v_max_f32_e32 v15, 0, v2
	v_accvgpr_read_b32 v2, a59
	v_add_f32_e32 v2, v5, v2
	v_max_f32_e32 v16, 0, v2
	ds_read_b128 v[2:5], v22 offset:53600
	s_waitcnt lgkmcnt(0)
	v_add_f32_e32 v2, v17, v2
	v_max_f32_e32 v17, 0, v2
	v_accvgpr_read_b32 v2, a61
	v_add_f32_e32 v2, v3, v2
	v_max_f32_e32 v18, 0, v2
	v_accvgpr_read_b32 v2, a62
	v_add_f32_e32 v2, v4, v2
	v_max_f32_e32 v19, 0, v2
	v_accvgpr_read_b32 v2, a63
	v_add_f32_e32 v2, v5, v2
	v_max_f32_e32 v20, 0, v2
	v_cvt_pk_f16_f32 v4, v9, v10
	v_cvt_pk_f16_f32 v3, v7, v8
	v_cvt_pk_f16_f32 v2, v1, v6
	ds_read_b128 v[6:9], v0 offset:45056
	v_cvt_pk_f16_f32 v5, v11, v12
	v_accvgpr_read_b32 v1, a32
	s_waitcnt lgkmcnt(0)
	v_mfma_f32_32x32x16_f16 a[80:95], v[6:9], v[2:5], a[80:95]
	ds_read_b128 v[6:9], v0 offset:46080
	v_cvt_pk_f16_f32 v5, v19, v20
	v_cvt_pk_f16_f32 v4, v17, v18
	v_cvt_pk_f16_f32 v3, v15, v16
	v_cvt_pk_f16_f32 v2, v13, v14
	v_accvgpr_read_b32 v13, a40
	v_accvgpr_read_b32 v17, a44
	s_waitcnt lgkmcnt(0)
	v_mfma_f32_32x32x16_f16 a[80:95], v[6:9], v[2:5], a[80:95]
	ds_read_b128 v[2:5], v22 offset:53632
	v_accvgpr_read_b32 v9, a36
	s_waitcnt lgkmcnt(0)
	v_add_f32_e32 v1, v1, v2
	v_accvgpr_read_b32 v2, a33
	v_add_f32_e32 v2, v3, v2
	v_max_f32_e32 v6, 0, v2
	v_accvgpr_read_b32 v2, a34
	v_add_f32_e32 v2, v4, v2
	v_max_f32_e32 v7, 0, v2
	v_accvgpr_read_b32 v2, a35
	v_add_f32_e32 v2, v5, v2
	v_max_f32_e32 v8, 0, v2
	ds_read_b128 v[2:5], v22 offset:53664
	v_max_f32_e32 v1, 0, v1
	s_waitcnt lgkmcnt(0)
	v_add_f32_e32 v2, v9, v2
	v_max_f32_e32 v9, 0, v2
	v_accvgpr_read_b32 v2, a37
	v_add_f32_e32 v2, v3, v2
	v_max_f32_e32 v10, 0, v2
	v_accvgpr_read_b32 v2, a38
	v_add_f32_e32 v2, v4, v2
	v_max_f32_e32 v11, 0, v2
	v_accvgpr_read_b32 v2, a39
	v_add_f32_e32 v2, v5, v2
	v_max_f32_e32 v12, 0, v2
	ds_read_b128 v[2:5], v22 offset:53696
	s_waitcnt lgkmcnt(0)
	v_add_f32_e32 v2, v13, v2
	v_max_f32_e32 v13, 0, v2
	v_accvgpr_read_b32 v2, a41
	v_add_f32_e32 v2, v3, v2
	v_max_f32_e32 v14, 0, v2
	v_accvgpr_read_b32 v2, a42
	v_add_f32_e32 v2, v4, v2
	v_max_f32_e32 v15, 0, v2
	v_accvgpr_read_b32 v2, a43
	v_add_f32_e32 v2, v5, v2
	v_max_f32_e32 v16, 0, v2
	ds_read_b128 v[2:5], v22 offset:53728
	s_waitcnt lgkmcnt(0)
	v_add_f32_e32 v2, v17, v2
	v_max_f32_e32 v17, 0, v2
	v_accvgpr_read_b32 v2, a45
	v_add_f32_e32 v2, v3, v2
	v_max_f32_e32 v18, 0, v2
	v_accvgpr_read_b32 v2, a46
	v_add_f32_e32 v2, v4, v2
	v_max_f32_e32 v19, 0, v2
	v_accvgpr_read_b32 v2, a47
	v_add_f32_e32 v2, v5, v2
	v_max_f32_e32 v20, 0, v2
	v_cvt_pk_f16_f32 v4, v9, v10
	v_cvt_pk_f16_f32 v3, v7, v8
	v_cvt_pk_f16_f32 v2, v1, v6
	ds_read_b128 v[6:9], v0 offset:47104
	v_cvt_pk_f16_f32 v5, v11, v12
	v_accvgpr_read_b32 v1, a16
	s_waitcnt lgkmcnt(0)
	v_mfma_f32_32x32x16_f16 a[32:47], v[6:9], v[2:5], 0
	ds_read_b128 v[6:9], v0 offset:48128
	v_cvt_pk_f16_f32 v5, v19, v20
	v_cvt_pk_f16_f32 v4, v17, v18
	v_cvt_pk_f16_f32 v3, v15, v16
	v_cvt_pk_f16_f32 v2, v13, v14
	v_accvgpr_read_b32 v13, a24
	v_accvgpr_read_b32 v17, a28
	s_waitcnt lgkmcnt(0)
	v_mfma_f32_32x32x16_f16 a[32:47], v[6:9], v[2:5], a[32:47]
	ds_read_b128 v[2:5], v22 offset:53760
	v_accvgpr_read_b32 v9, a20
	s_waitcnt lgkmcnt(0)
	v_add_f32_e32 v1, v1, v2
	v_accvgpr_read_b32 v2, a17
	v_add_f32_e32 v2, v3, v2
	v_max_f32_e32 v6, 0, v2
	v_accvgpr_read_b32 v2, a18
	v_add_f32_e32 v2, v4, v2
	v_max_f32_e32 v7, 0, v2
	v_accvgpr_read_b32 v2, a19
	v_add_f32_e32 v2, v5, v2
	v_max_f32_e32 v8, 0, v2
	ds_read_b128 v[2:5], v22 offset:53792
	v_max_f32_e32 v1, 0, v1
	s_waitcnt lgkmcnt(0)
	v_add_f32_e32 v2, v9, v2
	v_max_f32_e32 v9, 0, v2
	v_accvgpr_read_b32 v2, a21
	v_add_f32_e32 v2, v3, v2
	v_max_f32_e32 v10, 0, v2
	v_accvgpr_read_b32 v2, a22
	v_add_f32_e32 v2, v4, v2
	v_max_f32_e32 v11, 0, v2
	v_accvgpr_read_b32 v2, a23
	v_add_f32_e32 v2, v5, v2
	v_max_f32_e32 v12, 0, v2
	ds_read_b128 v[2:5], v22 offset:53824
	s_waitcnt lgkmcnt(0)
	v_add_f32_e32 v2, v13, v2
	v_max_f32_e32 v13, 0, v2
	v_accvgpr_read_b32 v2, a25
	v_add_f32_e32 v2, v3, v2
	v_max_f32_e32 v14, 0, v2
	v_accvgpr_read_b32 v2, a26
	v_add_f32_e32 v2, v4, v2
	v_max_f32_e32 v15, 0, v2
	v_accvgpr_read_b32 v2, a27
	v_add_f32_e32 v2, v5, v2
	v_max_f32_e32 v16, 0, v2
	ds_read_b128 v[2:5], v22 offset:53856
	s_waitcnt lgkmcnt(0)
	v_add_f32_e32 v2, v17, v2
	v_max_f32_e32 v17, 0, v2
	v_accvgpr_read_b32 v2, a29
	v_add_f32_e32 v2, v3, v2
	v_max_f32_e32 v18, 0, v2
	v_accvgpr_read_b32 v2, a30
	v_add_f32_e32 v2, v4, v2
	v_max_f32_e32 v19, 0, v2
	v_accvgpr_read_b32 v2, a31
	v_add_f32_e32 v2, v5, v2
	v_max_f32_e32 v20, 0, v2
	v_cvt_pk_f16_f32 v4, v9, v10
	v_cvt_pk_f16_f32 v3, v7, v8
	v_cvt_pk_f16_f32 v2, v1, v6
	ds_read_b128 v[6:9], v0 offset:49152
	v_cvt_pk_f16_f32 v5, v11, v12
	v_accvgpr_read_b32 v1, a0
	s_waitcnt lgkmcnt(0)
	v_mfma_f32_32x32x16_f16 a[32:47], v[6:9], v[2:5], a[32:47]
	ds_read_b128 v[6:9], v0 offset:50176
	v_cvt_pk_f16_f32 v5, v19, v20
	v_cvt_pk_f16_f32 v4, v17, v18
	v_cvt_pk_f16_f32 v3, v15, v16
	v_cvt_pk_f16_f32 v2, v13, v14
	v_accvgpr_read_b32 v13, a8
	v_accvgpr_read_b32 v17, a12
	s_waitcnt lgkmcnt(0)
	v_mfma_f32_32x32x16_f16 a[32:47], v[6:9], v[2:5], a[32:47]
	ds_read_b128 v[2:5], v22 offset:53888
	v_accvgpr_read_b32 v9, a4
	s_waitcnt lgkmcnt(0)
	v_add_f32_e32 v1, v1, v2
	v_accvgpr_read_b32 v2, a1
	v_add_f32_e32 v2, v3, v2
	v_max_f32_e32 v6, 0, v2
	v_accvgpr_read_b32 v2, a2
	v_add_f32_e32 v2, v4, v2
	v_max_f32_e32 v7, 0, v2
	v_accvgpr_read_b32 v2, a3
	v_add_f32_e32 v2, v5, v2
	v_max_f32_e32 v8, 0, v2
	ds_read_b128 v[2:5], v22 offset:53920
	v_max_f32_e32 v1, 0, v1
	s_waitcnt lgkmcnt(0)
	v_add_f32_e32 v2, v9, v2
	v_max_f32_e32 v9, 0, v2
	v_accvgpr_read_b32 v2, a5
	v_add_f32_e32 v2, v3, v2
	v_max_f32_e32 v10, 0, v2
	v_accvgpr_read_b32 v2, a6
	v_add_f32_e32 v2, v4, v2
	v_max_f32_e32 v11, 0, v2
	v_accvgpr_read_b32 v2, a7
	v_add_f32_e32 v2, v5, v2
	v_max_f32_e32 v12, 0, v2
	ds_read_b128 v[2:5], v22 offset:53952
	s_waitcnt lgkmcnt(0)
	v_add_f32_e32 v2, v13, v2
	v_max_f32_e32 v13, 0, v2
	v_accvgpr_read_b32 v2, a9
	v_add_f32_e32 v2, v3, v2
	v_max_f32_e32 v14, 0, v2
	v_accvgpr_read_b32 v2, a10
	v_add_f32_e32 v2, v4, v2
	v_max_f32_e32 v15, 0, v2
	v_accvgpr_read_b32 v2, a11
	v_add_f32_e32 v2, v5, v2
	v_max_f32_e32 v16, 0, v2
	ds_read_b128 v[2:5], v22 offset:53984
	s_waitcnt lgkmcnt(0)
	v_add_f32_e32 v2, v17, v2
	v_max_f32_e32 v17, 0, v2
	v_accvgpr_read_b32 v2, a13
	v_add_f32_e32 v2, v3, v2
	v_max_f32_e32 v18, 0, v2
	v_accvgpr_read_b32 v2, a14
	v_add_f32_e32 v2, v4, v2
	v_max_f32_e32 v19, 0, v2
	v_accvgpr_read_b32 v2, a15
	v_add_f32_e32 v2, v5, v2
	v_max_f32_e32 v20, 0, v2
	v_cvt_pk_f16_f32 v4, v9, v10
	v_cvt_pk_f16_f32 v3, v7, v8
	v_cvt_pk_f16_f32 v2, v1, v6
	ds_read_b128 v[6:9], v0 offset:51200
	v_cvt_pk_f16_f32 v5, v11, v12
	s_waitcnt lgkmcnt(0)
	s_nop 0
	v_mfma_f32_32x32x16_f16 a[32:47], v[6:9], v[2:5], a[32:47]
	ds_read_b128 v[6:9], v0 offset:52224
	v_cvt_pk_f16_f32 v5, v19, v20
	v_cvt_pk_f16_f32 v4, v17, v18
	v_cvt_pk_f16_f32 v3, v15, v16
	v_cvt_pk_f16_f32 v2, v13, v14
	s_waitcnt lgkmcnt(0)
	s_nop 0
	v_mfma_f32_32x32x16_f16 a[32:47], v[6:9], v[2:5], a[32:47]
	s_and_saveexec_b64 s[2:3], s[0:1]
	s_cbranch_execz .LBB3_39
	v_accvgpr_read_b32 v0, a80
	v_accvgpr_read_b32 v6, a86
	v_accvgpr_read_b32 v7, a87
	v_accvgpr_read_b32 v8, a88
	v_accvgpr_read_b32 v9, a89
	v_accvgpr_read_b32 v10, a90
	v_accvgpr_read_b32 v11, a91
	v_accvgpr_read_b32 v12, a92
	v_accvgpr_read_b32 v13, a93
	v_accvgpr_read_b32 v14, a94
	v_accvgpr_read_b32 v15, a95
	v_accvgpr_read_b32 v6, a32
	v_accvgpr_read_b32 v14, a40
	v_accvgpr_read_b32 v15, a41
	v_accvgpr_read_b32 v16, a42
	v_accvgpr_read_b32 v17, a43
	v_accvgpr_read_b32 v18, a44
	v_accvgpr_read_b32 v19, a45
	v_accvgpr_read_b32 v20, a46
	v_accvgpr_read_b32 v21, a47
	ds_read_b128 v[14:17], v22 offset:54016
	ds_read_b128 v[18:21], v22 offset:54080
	v_accvgpr_read_b32 v12, a38
	v_accvgpr_read_b32 v13, a39
	v_lshlrev_b32_e32 v24, 2, v85
	v_accvgpr_read_b32 v1, a81
	v_accvgpr_read_b32 v7, a33
	v_mad_i64_i32 v[12:13], s[0:1], v80, 40, s[18:19]
	v_ashrrev_i32_e32 v25, 31, v24
	v_accvgpr_read_b32 v3, a83
	v_accvgpr_read_b32 v9, a35
	v_lshl_add_u64 v[22:23], v[24:25], 2, v[12:13]
	v_mov_b32_e32 v25, v1
	s_waitcnt lgkmcnt(1)
	v_mov_b32_e32 v27, v15
	v_mov_b32_e32 v1, v7
	s_waitcnt lgkmcnt(0)
	v_mov_b32_e32 v15, v19
	v_accvgpr_read_b32 v2, a82
	v_accvgpr_read_b32 v8, a34
	v_pk_add_f32 v[0:1], v[0:1], v[14:15]
	v_mov_b32_e32 v7, v3
	v_mov_b32_e32 v15, v17
	v_mov_b32_e32 v3, v9
	v_mov_b32_e32 v17, v21
	v_mov_b32_e32 v24, v6
	v_mov_b32_e32 v26, v18
	v_mov_b32_e32 v6, v8
	v_mov_b32_e32 v14, v20
	v_pk_add_f32 v[2:3], v[2:3], v[16:17]
	v_pk_add_f32 v[24:25], v[24:25], v[26:27]
	s_waitcnt vmcnt(0)
	v_pk_mul_f32 v[0:1], v[82:83], v[0:1]
	v_pk_add_f32 v[6:7], v[6:7], v[14:15]
	v_pk_mul_f32 v[2:3], v[82:83], v[2:3]
	v_accvgpr_read_b32 v4, a84
	v_accvgpr_read_b32 v5, a85
	v_accvgpr_read_b32 v10, a36
	v_accvgpr_read_b32 v11, a37
	v_pk_fma_f32 v[0:1], v[82:83], v[24:25], v[0:1] op_sel:[1,0,0] op_sel_hi:[0,1,1]
	v_pk_fma_f32 v[2:3], v[82:83], v[6:7], v[2:3] op_sel:[1,0,0] op_sel_hi:[0,1,1]
	v_cmp_eq_u32_e32 vcc, 0, v85
	global_store_dwordx4 v[22:23], v[0:3], off
	s_and_b64 exec, exec, vcc
	s_cbranch_execz .LBB3_39
	s_mov_b32 s0, 0xd000
	v_add_u32_e64 v0, s0, 0
	ds_read2_b64 v[0:3], v0 offset0:100 offset1:108
	v_mov_b32_e32 v9, v5
	v_mov_b32_e32 v5, v11
	v_mov_b32_e32 v8, v10
	v_pk_mov_b32 v[6:7], v[82:83], v[82:83] op_sel:[1,0]
	s_waitcnt lgkmcnt(0)
	v_mov_b32_e32 v15, v1
	v_mov_b32_e32 v1, v3
	v_mov_b32_e32 v14, v2
	v_pk_add_f32 v[0:1], v[4:5], v[0:1]
	v_pk_add_f32 v[8:9], v[8:9], v[14:15]
	v_pk_mul_f32 v[0:1], v[82:83], v[0:1]
	s_nop 0
	v_pk_fma_f32 v[0:1], v[6:7], v[8:9], v[0:1]
	global_store_dwordx2 v[12:13], v[0:1], off offset:32
